# v26: v19 + LDS-DMA wrappers without the dead m0 save/restore
# speedup vs baseline: 1.0035x; 1.0007x over previous
; template <int MODE, int DQK, int DV>
; __device__ __forceinline__ void attn_pass(LAS unsigned char* lds, const Tens& T, size_t rowbase, int q0, f32x16 (&o)[DV / 32], float& l_out, const int wave, QPre* qp = nullptr) {
;     ...
;         const bf16* qp = T.Q + (rowbase + tq) * (size_t)T.ldq + 8 * h;
; #pragma unroll
;         for (int s = 0; s < NSTEP; ++s) qf[s] = *(const bf16x8*)(qp + 16 * s);
;     }
;     {
;         f32x4 c0 = {1.f, 1.f, 1.f, 1.f}, c1 = c0, s0 = {0.f, 0.f, 0.f, 0.f}, s1 = s0;
;         if (MODE == AM_MLA) {
;             c0 = *(const f32x4*)(T.rcos + tq * 16 + 8 * h); c1 = *(const f32x4*)(T.rcos + tq * 16 + 8 * h + 4);
;             s0 = *(const f32x4*)(T.rsin + tq * 16 + 8 * h); s1 = *(const f32x4*)(T.rsin + tq * 16 + 8 * h + 4);
;         }
; #pragma unroll
;         for (int s = 0; s < NSTEP; ++s) {
;             if (MODE == AM_MLA && s == NSTEP - 1) continue;
;             bf16x8 a = qf[s];
;             if (MODE == AM_MLA && s == NSTEP - 2) {
;                 bf16x8 b2 = qf[NSTEP - 1];
; #pragma unroll
;                 for (int j = 0; j < 8; ++j) {
;                     const float x1 = __uint_as_float(((unsigned)(unsigned short)a[j]) << 16), x2 = __uint_as_float(((unsigned)(unsigned short)b2[j]) << 16);
;                     const float cs = j < 4 ? c0[j & 3] : c1[j & 3], sn = j < 4 ? s0[j & 3] : s1[j & 3];
;                     a[j] = (short)f2bf((x1 * cs - x2 * sn) * T.scale2); b2[j] = (short)f2bf((x2 * cs + x1 * sn) * T.scale2);
;                 }
;                 qf[NSTEP - 1] = b2;
;             } else {
; #pragma unroll
; template <int PH>
; __device__ __forceinline__ void mk_body(const Args& a) {
;     ...
;             const int u = att::next_unit_pre(qp, ctl + CW_Q + 0 * 512, 256, lds, att::OFF_MISC, wave);
;             if (u < 0) break;
;             const int b = u >> 8, h = 2 * ((u >> 6) & 3) + ((u >> 4) & 1), qb = ((u >> 5) & 1) ? 15 - (u & 15) : 31 - (u & 15);
;             att::Tens T{};
;             T.Q = y0 + Y0_FQ + h * 64; T.ldq = Y0P; T.K = y0 + Y0_FK + h * 64; T.ldk = Y0P; T.V = y0 + Y0_FV + h * 64; T.ldv = Y0P;
;             T.lc = lcum + h; T.scale2 = 0.125f * att::LOG2E;
;             T.kmaxn = sqrtf(__uint_as_float(__hip_atomic_load(ctl + CW_KMAX + b * 8 + h, __ATOMIC_RELAXED, __HIP_MEMORY_SCOPE_AGENT)));
.LBB0_632:
	v_add_u32_e32 v0, 0, v0
	s_waitcnt lgkmcnt(0)
	s_barrier
	ds_read_b32 v0, v0
	s_waitcnt lgkmcnt(0)
	s_barrier
	v_readfirstlane_b32 s1, v0
	s_cmp_lt_i32 s1, 0
	s_cbranch_scc1 .LBB0_711
	s_lshr_b32 s2, s1, 5
	s_and_b32 s2, s2, 6
	s_bfe_u32 s3, s1, 0x10004
	s_lshr_b32 s44, s1, 8
	s_or_b32 s4, s2, s3
	s_and_b32 s2, s1, 32
	s_and_b32 s1, s1, 15
	s_cmp_eq_u32 s2, 0
	s_cselect_b32 s2, 31, 15
	s_xor_b32 s1, s2, s1
	s_lshl_b32 s2, s4, 7
	v_readlane_b32 s3, v254, 30
	s_add_u32 s10, s3, s2
	v_readlane_b32 s3, v254, 31
	s_addc_u32 s11, s3, 0
	v_readlane_b32 s3, v254, 33
	s_add_u32 s5, s3, s2
	v_readlane_b32 s3, v254, 35
	s_addc_u32 s6, s3, 0
	v_readlane_b32 s3, v254, 37
	s_add_u32 s7, s3, s2
	v_readlane_b32 s2, v254, 39
	s_addc_u32 s8, s2, 0
	s_lshl_b32 s9, s4, 2
	v_readlane_b32 s2, v254, 41
	s_add_u32 s2, s2, s9
	v_readlane_b32 s3, v254, 43
	s_addc_u32 s3, s3, 0
	s_lshl_b32 s12, s44, 5
	v_readlane_b32 s13, v254, 45
	s_add_u32 s12, s13, s12
	v_readlane_b32 s13, v254, 47
	s_addc_u32 s13, s13, 0
	v_mov_b32_e32 v0, s9
	s_lshl_b32 s83, s1, 8
	v_readlane_b32 s9, v254, 53
	s_add_i32 s82, s83, s9
	global_load_dword v3, v0, s[12:13] sc1
	v_mbcnt_lo_u32_b32 v46, -1, 0
	v_mbcnt_hi_u32_b32 v46, -1, v46
	s_lshl_b64 s[66:67], s[44:45], 13
	v_and_b32_e32 v0, 31, v46
	v_or_b32_e32 v82, s82, v0
	v_lshl_add_u64 v[36:37], s[66:67], 0, v[82:83]
	v_mov_b64_e32 v[4:5], s[10:11]
	s_movk_i32 s9, 0x1c00
	v_bfe_u32 v1, v46, 5, 1
	v_mad_u64_u32 v[4:5], s[10:11], v36, s9, v[4:5]
	v_mad_u32_u24 v5, v37, s9, v5
	v_lshlrev_b32_e32 v82, 4, v1
	v_lshl_add_u64 v[12:13], v[4:5], 0, v[82:83]
	global_load_dwordx4 v[4:7], v[12:13], off
	global_load_dwordx4 v[8:11], v[12:13], off offset:32
	global_load_dwordx4 v[24:27], v[12:13], off offset:64
	global_load_dwordx4 v[32:35], v[12:13], off offset:96
	v_lshlrev_b64 v[36:37], 5, v[36:37]
	v_lshl_add_u64 v[36:37], s[2:3], 0, v[36:37]
	global_load_dword v36, v[36:37], off
	s_add_i32 s9, s83, 0x100
	s_lshr_b32 s84, s9, 6
	v_readlane_b32 s9, v254, 49
	s_lshl_b64 s[10:11], s[44:45], 18
	v_and_b32_e32 v2, 63, v46
	v_lshlrev_b32_e32 v99, 5, v2
	s_waitcnt vmcnt(0)
	v_and_b32_e32 v13, 0xffff0000, v4
	v_lshlrev_b32_e32 v12, 16, v4
	v_and_b32_e32 v15, 0xffff0000, v5
	v_lshlrev_b32_e32 v14, 16, v5
	v_and_b32_e32 v5, 0xffff0000, v6
	v_lshlrev_b32_e32 v4, 16, v6
	v_and_b32_e32 v17, 0xffff0000, v7
	v_lshlrev_b32_e32 v16, 16, v7
	v_and_b32_e32 v7, 0xffff0000, v8
	v_lshlrev_b32_e32 v6, 16, v8
	v_and_b32_e32 v19, 0xffff0000, v9
	v_lshlrev_b32_e32 v18, 16, v9
	v_and_b32_e32 v9, 0xffff0000, v10
	v_lshlrev_b32_e32 v8, 16, v10
	v_and_b32_e32 v21, 0xffff0000, v11
	v_lshlrev_b32_e32 v20, 16, v11
	v_and_b32_e32 v11, 0xffff0000, v24
	v_lshlrev_b32_e32 v10, 16, v24
	v_pk_mul_f32 v[12:13], v[12:13], s[48:49] op_sel_hi:[1,0]
	v_pk_mul_f32 v[14:15], v[14:15], s[48:49] op_sel_hi:[1,0]
	v_pk_mul_f32 v[22:23], v[4:5], s[48:49] op_sel_hi:[1,0]
	v_pk_mul_f32 v[30:31], v[6:7], s[48:49] op_sel_hi:[1,0]
	v_pk_mul_f32 v[40:41], v[8:9], s[48:49] op_sel_hi:[1,0]
	v_pk_mul_f32 v[44:45], v[10:11], s[48:49] op_sel_hi:[1,0]
	v_and_b32_sdwa v5, v12, v90 dst_sel:DWORD dst_unused:UNUSED_PAD src0_sel:WORD_1 src1_sel:DWORD
	v_and_b32_sdwa v8, v14, v90 dst_sel:DWORD dst_unused:UNUSED_PAD src0_sel:WORD_1 src1_sel:DWORD
	v_and_b32_sdwa v9, v23, v90 dst_sel:DWORD dst_unused:UNUSED_PAD src0_sel:WORD_1 src1_sel:DWORD
	v_and_b32_sdwa v11, v22, v90 dst_sel:DWORD dst_unused:UNUSED_PAD src0_sel:WORD_1 src1_sel:DWORD
	v_pk_mul_f32 v[28:29], v[16:17], s[48:49] op_sel_hi:[1,0]
	v_and_b32_sdwa v24, v30, v90 dst_sel:DWORD dst_unused:UNUSED_PAD src0_sel:WORD_1 src1_sel:DWORD
	v_add3_u32 v7, v12, v5, s97
	v_add3_u32 v12, v14, v8, s97
	v_add3_u32 v14, v23, v9, s97
	v_add3_u32 v16, v22, v11, s97
	v_and_b32_e32 v23, 0xffff0000, v25
	v_lshlrev_b32_e32 v22, 16, v25
	v_add3_u32 v8, v30, v24, s97
	v_pk_mul_f32 v[24:25], v[22:23], s[48:49] op_sel_hi:[1,0]
	v_pk_mul_f32 v[38:39], v[18:19], s[48:49] op_sel_hi:[1,0]
	v_and_b32_sdwa v22, v25, v90 dst_sel:DWORD dst_unused:UNUSED_PAD src0_sel:WORD_1 src1_sel:DWORD
	v_and_b32_sdwa v23, v24, v90 dst_sel:DWORD dst_unused:UNUSED_PAD src0_sel:WORD_1 src1_sel:DWORD
	v_and_b32_sdwa v17, v29, v90 dst_sel:DWORD dst_unused:UNUSED_PAD src0_sel:WORD_1 src1_sel:DWORD
	v_and_b32_sdwa v19, v28, v90 dst_sel:DWORD dst_unused:UNUSED_PAD src0_sel:WORD_1 src1_sel:DWORD
	v_add3_u32 v22, v25, v22, s97
	v_add3_u32 v23, v24, v23, s97
	v_and_b32_e32 v25, 0xffff0000, v26
	v_lshlrev_b32_e32 v24, 16, v26
	v_pk_mul_f32 v[42:43], v[20:21], s[48:49] op_sel_hi:[1,0]
	v_add3_u32 v18, v29, v17, s97
	v_add3_u32 v20, v28, v19, s97
	v_pk_mul_f32 v[28:29], v[24:25], s[48:49] op_sel_hi:[1,0]
	v_and_b32_sdwa v21, v31, v90 dst_sel:DWORD dst_unused:UNUSED_PAD src0_sel:WORD_1 src1_sel:DWORD
	v_and_b32_sdwa v24, v29, v90 dst_sel:DWORD dst_unused:UNUSED_PAD src0_sel:WORD_1 src1_sel:DWORD
	v_and_b32_sdwa v25, v28, v90 dst_sel:DWORD dst_unused:UNUSED_PAD src0_sel:WORD_1 src1_sel:DWORD
	v_add3_u32 v24, v29, v24, s97
	v_add3_u32 v25, v28, v25, s97
	v_and_b32_e32 v29, 0xffff0000, v27
	v_lshlrev_b32_e32 v28, 16, v27
	v_pk_mul_f32 v[26:27], v[28:29], s[48:49] op_sel_hi:[1,0]
	v_add3_u32 v5, v31, v21, s97
	v_and_b32_sdwa v28, v27, v90 dst_sel:DWORD dst_unused:UNUSED_PAD src0_sel:WORD_1 src1_sel:DWORD
	v_and_b32_sdwa v29, v26, v90 dst_sel:DWORD dst_unused:UNUSED_PAD src0_sel:WORD_1 src1_sel:DWORD
	v_add3_u32 v28, v27, v28, s97
	v_add3_u32 v29, v26, v29, s97
	v_and_b32_e32 v27, 0xffff0000, v32
	v_lshlrev_b32_e32 v26, 16, v32
	v_pk_mul_f32 v[30:31], v[26:27], s[48:49] op_sel_hi:[1,0]
	v_and_b32_sdwa v4, v13, v90 dst_sel:DWORD dst_unused:UNUSED_PAD src0_sel:WORD_1 src1_sel:DWORD
; #define LAS __attribute__((address_space(3)))
; template <int MODE, int DQK, int DV>
; __device__ __forceinline__ void attn_pass(LAS unsigned char* lds, const Tens& T, size_t rowbase, int q0, f32x16 (&o)[DV / 32], float& l_out, const int wave, QPre* qp = nullptr) {
;     ...
;             for (int j = 0; j < 8; ++j) { const float v = __uint_as_float(((unsigned)(unsigned short)qf[s][j]) << 16); qs = fmaf(v, v, qs); }
;         qs = sum32f(qs);
;         bq = sqrtf(qs) * T.kmaxn * 1.001f + 1.0f;
;     }
;     const LAS float* lut = (const LAS float*)(lds + OFF_LUT);
;     const int dk_key = 8 * wave + (lane >> 3), dk_col = ((lane & 7) ^ ((dk_key >> 1) & 7)) * 8;
;     const int dr_key = 16 * wave + (lane >> 2), dr_col = ((lane & 3) ^ ((dr_key >> 2) & 3)) * 8;
;     int dv_key[DV / 64], dv_col[DV / 64];
; #pragma unroll
;     for (int n = 0; n < DV / 64; ++n) {
;         if (DV == 64) { dv_key[n] = 8 * wave + (lane >> 3); const int pos = lane & 7; dv_col[n] = (((pos >> 2) ^ ((dv_key[n] >> 1) & 1)) * 32) + (pos & 3) * 8; }
;         else          { dv_key[n] = 8 * wave + 4 * n + (lane >> 4); const int pos = lane & 15; dv_col[n] = (((pos >> 2) ^ (dv_key[n] & 3)) * 32) + (pos & 3) * 8; }
;     }
;     const int dm_q = (wave * 64 + lane) >> 1, dm_kb = lane & 1;
;     const unsigned lds0 = (unsigned)(uintptr_t)lds;
;     ...
;     const unsigned kvo = (unsigned)(dk_key * T.ldk + dk_col) * 2u, rvo = (unsigned)(dr_key * T.ldk2 + dr_col) * 2u;
;     unsigned vvo[DV / 64];
; #pragma unroll
;     for (int n = 0; n < DV / 64; ++n) vvo[n] = (unsigned)(dv_key[n] * T.ldv + dv_col[n]) * 2u;
;     const unsigned cvo = (unsigned)lane * 32u, mvo = (unsigned)(wave * 64 + lane) * 4u;
;     const char* const ubK = (const char*)(T.K + rowbase * (size_t)T.ldk);
;     const char* const ubK2 = (MODE == AM_MLA) ? (const char*)(T.K2 + rowbase * (size_t)T.ldk2) : nullptr;
;     const char* const ubV = (const char*)(T.V + rowbase * (size_t)T.ldv);
;     const char* const ubC = (MODE == AM_FOX) ? (const char*)(T.lc + rowbase * 8) : nullptr;
;     const char* const ubM = (MODE == AM_DSA) ? (const char*)(T.mask + ((rowbase / S * 128) * (size_t)S + q0) * 2) : nullptr;
;     ...
;     const int nvm = 1 + ((DQK == 96 && wave < 4) ? 1 : 0) + DV / 64 + ((MODE == AM_FOX && wave == 0) ? 1 : 0) + ((MODE == AM_DSA) ? 1 : 0);
	v_and_b32_sdwa v26, v31, v90 dst_sel:DWORD dst_unused:UNUSED_PAD src0_sel:WORD_1 src1_sel:DWORD
	v_and_b32_sdwa v27, v30, v90 dst_sel:DWORD dst_unused:UNUSED_PAD src0_sel:WORD_1 src1_sel:DWORD
	v_add3_u32 v26, v31, v26, s97
	v_add3_u32 v27, v30, v27, s97
	v_and_b32_e32 v31, 0xffff0000, v33
	v_lshlrev_b32_e32 v30, 16, v33
	v_pk_mul_f32 v[32:33], v[30:31], s[48:49] op_sel_hi:[1,0]
	v_and_b32_sdwa v47, v39, v90 dst_sel:DWORD dst_unused:UNUSED_PAD src0_sel:WORD_1 src1_sel:DWORD
	v_and_b32_sdwa v30, v33, v90 dst_sel:DWORD dst_unused:UNUSED_PAD src0_sel:WORD_1 src1_sel:DWORD
	v_and_b32_sdwa v31, v32, v90 dst_sel:DWORD dst_unused:UNUSED_PAD src0_sel:WORD_1 src1_sel:DWORD
	v_and_b32_sdwa v48, v38, v90 dst_sel:DWORD dst_unused:UNUSED_PAD src0_sel:WORD_1 src1_sel:DWORD
	v_add3_u32 v30, v33, v30, s97
	v_add3_u32 v31, v32, v31, s97
	v_and_b32_e32 v33, 0xffff0000, v34
	v_lshlrev_b32_e32 v32, 16, v34
	v_add3_u32 v4, v13, v4, s97
	v_add3_u32 v11, v39, v47, s97
	v_add3_u32 v13, v38, v48, s97
	v_pk_mul_f32 v[38:39], v[32:33], s[48:49] op_sel_hi:[1,0]
	v_and_b32_e32 v37, 0xffff0000, v7
	v_and_b32_sdwa v32, v39, v90 dst_sel:DWORD dst_unused:UNUSED_PAD src0_sel:WORD_1 src1_sel:DWORD
	v_and_b32_sdwa v33, v38, v90 dst_sel:DWORD dst_unused:UNUSED_PAD src0_sel:WORD_1 src1_sel:DWORD
	v_add3_u32 v32, v39, v32, s97
	v_add3_u32 v33, v38, v33, s97
	v_and_b32_e32 v39, 0xffff0000, v35
	v_lshlrev_b32_e32 v38, 16, v35
	v_pk_mul_f32 v[38:39], v[38:39], s[48:49] op_sel_hi:[1,0]
	v_and_b32_sdwa v6, v15, v90 dst_sel:DWORD dst_unused:UNUSED_PAD src0_sel:WORD_1 src1_sel:DWORD
	v_and_b32_sdwa v35, v38, v90 dst_sel:DWORD dst_unused:UNUSED_PAD src0_sel:WORD_1 src1_sel:DWORD
	v_add3_u32 v35, v38, v35, s97
	v_fma_f32 v37, v37, v37, 0
	v_and_b32_e32 v38, 0xffff0000, v4
	v_add3_u32 v10, v15, v6, s97
	v_fmac_f32_e32 v37, v38, v38
	v_and_b32_e32 v38, 0xffff0000, v12
	v_fmac_f32_e32 v37, v38, v38
	v_and_b32_e32 v38, 0xffff0000, v10
	v_fmac_f32_e32 v37, v38, v38
	v_and_b32_e32 v38, 0xffff0000, v16
	v_fmac_f32_e32 v37, v38, v38
	v_and_b32_e32 v38, 0xffff0000, v14
	v_fmac_f32_e32 v37, v38, v38
	v_and_b32_e32 v38, 0xffff0000, v20
	v_fmac_f32_e32 v37, v38, v38
	v_and_b32_e32 v38, 0xffff0000, v18
	v_fmac_f32_e32 v37, v38, v38
	v_and_b32_e32 v38, 0xffff0000, v8
	v_fmac_f32_e32 v37, v38, v38
	v_and_b32_e32 v38, 0xffff0000, v5
	v_and_b32_sdwa v50, v40, v90 dst_sel:DWORD dst_unused:UNUSED_PAD src0_sel:WORD_1 src1_sel:DWORD
	v_fmac_f32_e32 v37, v38, v38
	v_and_b32_e32 v38, 0xffff0000, v13
	v_and_b32_sdwa v49, v41, v90 dst_sel:DWORD dst_unused:UNUSED_PAD src0_sel:WORD_1 src1_sel:DWORD
	v_add3_u32 v17, v40, v50, s97
	v_fmac_f32_e32 v37, v38, v38
	v_and_b32_e32 v38, 0xffff0000, v11
	v_and_b32_sdwa v52, v42, v90 dst_sel:DWORD dst_unused:UNUSED_PAD src0_sel:WORD_1 src1_sel:DWORD
	v_add3_u32 v15, v41, v49, s97
	v_fmac_f32_e32 v37, v38, v38
	v_and_b32_e32 v38, 0xffff0000, v17
	v_and_b32_sdwa v51, v43, v90 dst_sel:DWORD dst_unused:UNUSED_PAD src0_sel:WORD_1 src1_sel:DWORD
	v_add3_u32 v21, v42, v52, s97
	v_fmac_f32_e32 v37, v38, v38
	v_and_b32_e32 v38, 0xffff0000, v15
	v_and_b32_sdwa v54, v44, v90 dst_sel:DWORD dst_unused:UNUSED_PAD src0_sel:WORD_1 src1_sel:DWORD
	v_add3_u32 v19, v43, v51, s97
	v_and_b32_sdwa v34, v39, v90 dst_sel:DWORD dst_unused:UNUSED_PAD src0_sel:WORD_1 src1_sel:DWORD
	v_fmac_f32_e32 v37, v38, v38
	v_and_b32_e32 v38, 0xffff0000, v21
	v_and_b32_sdwa v53, v45, v90 dst_sel:DWORD dst_unused:UNUSED_PAD src0_sel:WORD_1 src1_sel:DWORD
	v_add3_u32 v9, v44, v54, s97
	v_add3_u32 v34, v39, v34, s97
	v_fmac_f32_e32 v37, v38, v38
	v_and_b32_e32 v38, 0xffff0000, v19
	v_bfe_u32 v39, v46, 3, 3
	v_add3_u32 v6, v45, v53, s97
	v_fmac_f32_e32 v37, v38, v38
	v_and_b32_e32 v38, 0xffff0000, v9
	v_or_b32_e32 v40, s9, v39
	v_lshrrev_b32_e32 v42, 4, v46
	v_lshrrev_b32_e32 v43, 2, v46
	v_fmac_f32_e32 v37, v38, v38
	v_and_b32_e32 v38, 0xffff0000, v6
	v_lshrrev_b32_e32 v41, 1, v40
	v_xor_b32_e32 v42, v43, v42
	v_fmac_f32_e32 v37, v38, v38
	v_and_b32_e32 v38, 0xffff0000, v23
	v_xor_b32_e32 v41, v41, v46
	v_lshlrev_b32_e32 v42, 5, v42
	v_lshlrev_b32_e32 v43, 3, v46
	s_movk_i32 s9, 0xe00
	v_fmac_f32_e32 v37, v38, v38
	v_and_b32_e32 v38, 0xffff0000, v22
	v_lshlrev_b32_e32 v41, 3, v41
	v_and_b32_e32 v42, 32, v42
	v_and_b32_e32 v44, 24, v43
	v_mul_lo_u32 v40, v40, s9
	v_fmac_f32_e32 v37, v38, v38
	v_and_b32_e32 v38, 0xffff0000, v25
	v_and_or_b32 v41, v41, 56, v40
	v_or3_b32 v40, v44, v42, v40
	v_bfe_u32 v45, v46, 2, 2
	v_fmac_f32_e32 v37, v38, v38
	v_and_b32_e32 v38, 0xffff0000, v24
	v_lshlrev_b32_e32 v94, 1, v40
	v_lshlrev_b32_e32 v40, 2, v46
	v_and_or_b32 v39, v39, 4, v45
	v_and_b32_e32 v45, 16, v46
	v_fmac_f32_e32 v37, v38, v38
	v_and_b32_e32 v38, 0xffff0000, v29
	s_add_u32 s9, s2, s10
	v_and_or_b32 v40, v40, 12, v45
	v_fmac_f32_e32 v37, v38, v38
	v_and_b32_e32 v38, 0xffff0000, v28
	s_addc_u32 s10, s3, s11
	s_mul_i32 s3, s44, 0x3800000
	v_lshlrev_b32_e32 v39, 7, v39
	v_lshlrev_b32_e32 v40, 1, v40
	v_fmac_f32_e32 v37, v38, v38
	v_and_b32_e32 v38, 0xffff0000, v27
	s_mul_hi_u32 s2, s44, 0x3800000
	s_add_u32 s7, s7, s3
	v_add3_u32 v39, 0, v39, v40
	v_and_b32_e32 v40, 64, v43
	s_movk_i32 s11, 0x6000
	v_fmac_f32_e32 v37, v38, v38
	v_and_b32_e32 v38, 0xffff0000, v26
	v_lshrrev_b32_e32 v42, 1, v46
	s_addc_u32 s8, s8, s2
	v_add3_u32 v100, v39, v40, s11
	v_bitop3_b32 v40, v43, 64, v43 bitop3:0xc
	v_fmac_f32_e32 v37, v38, v38
	v_and_b32_e32 v38, 0xffff0000, v31
	v_bfe_u32 v44, v46, 1, 3
	v_lshl_add_u32 v45, v0, 7, 0
	v_bitop3_b32 v42, v1, v42, 7 bitop3:0x78
	v_add3_u32 v101, v39, v40, s11
	s_add_u32 s11, s5, s3
	v_fmac_f32_e32 v37, v38, v38
	v_and_b32_e32 v38, 0xffff0000, v30
	v_lshl_add_u32 v95, v42, 4, v45
	v_bitop3_b32 v42, v1, v44, 2 bitop3:0x36
	s_addc_u32 s6, s6, s2
	s_add_i32 s44, s84, -1
	v_fmac_f32_e32 v37, v38, v38
	v_and_b32_e32 v38, 0xffff0000, v33
	v_lshl_add_u32 v96, v42, 4, v45
	v_bitop3_b32 v42, v1, v44, 4 bitop3:0x36
	s_mul_i32 s12, s44, 0x70000
	v_fmac_f32_e32 v37, v38, v38
	v_and_b32_e32 v38, 0xffff0000, v32
	v_lshl_add_u32 v97, v42, 4, v45
	v_bitop3_b32 v42, v1, v44, 6 bitop3:0x36
	s_mul_hi_u32 s5, s44, 0x70000
	s_add_u32 s2, s11, s12
	v_fmac_f32_e32 v37, v38, v38
	v_and_b32_e32 v38, 0xffff0000, v35
	v_lshl_add_u32 v98, v42, 4, v45
	s_addc_u32 s3, s6, s5
	v_fmac_f32_e32 v37, v38, v38
	v_and_b32_e32 v38, 0xffff0000, v34
	v_lshlrev_b32_e32 v102, 1, v41
	s_mov_b32 m0, s80
	s_nop 0
	global_load_lds_dwordx4 v102, s[2:3]
	s_add_u32 s2, s7, s12
	v_fmac_f32_e32 v37, v38, v38
	s_addc_u32 s3, s8, s5
	v_readlane_b32 s12, v254, 26
	s_mov_b32 m0, s81
	s_nop 0
	global_load_lds_dwordx4 v94, s[2:3]
	v_mov_b32_e32 v38, v37
	v_readlane_b32 s13, v254, 27
	s_nop 0
	v_permlane32_swap_b32_e32 v37, v38
	s_and_b64 vcc, exec, s[12:13]
	s_cbranch_vccnz .LBB0_635
	s_lshl_b64 s[2:3], s[44:45], 11
	s_add_u32 s2, s9, s2
	s_addc_u32 s3, s10, s3
	v_readlane_b32 s12, v254, 57
	s_mov_b32 m0, s12
	s_nop 0
	global_load_lds_dword v99, s[2:3]
; #define ATT_ISSUE(st_, sl) do { _Pragma("unroll") for (int sb_ = 0; sb_ < NSUB; ++sb_) ATT_DMA(ATT_TILE((st_) * NSUB + sb_), sl, sb_); } while (0)
; #define ATT_WAIT_PREV() do { if (NSUB == 1) { if (nvm == 2) asm volatile("s_waitcnt vmcnt(2)" ::: "memory"); else asm volatile("s_waitcnt vmcnt(3)" ::: "memory"); } \
;                               else { if (nvm == 2) asm volatile("s_waitcnt vmcnt(4)" ::: "memory"); else asm volatile("s_waitcnt vmcnt(6)" ::: "memory"); } } while (0)
; #define ATT_BAR() asm volatile("s_waitcnt lgkmcnt(0)\n\ts_barrier" ::: "memory")
; template <int MODE, int DQK, int DV>
; __device__ __forceinline__ void attn_pass(LAS unsigned char* lds, const Tens& T, size_t rowbase, int q0, f32x16 (&o)[DV / 32], float& l_out, const int wave, QPre* qp = nullptr) {
;     ...
;     const int nvm = 1 + ((DQK == 96 && wave < 4) ? 1 : 0) + DV / 64 + ((MODE == AM_FOX && wave == 0) ? 1 : 0) + ((MODE == AM_DSA) ? 1 : 0);
;     ...
;     ATT_ISSUE(0, 0);
;     if (NRING == 3) ATT_ISSUE(1, 1);
;     if (NRING == 3) ATT_WAIT_PREV(); else asm volatile("s_waitcnt vmcnt(0)" ::: "memory");
;     ATT_BAR();
.LBB0_635:
	s_add_i32 s44, s84, -2
	s_mul_i32 s12, s44, 0x70000
	s_mul_hi_u32 s5, s44, 0x70000
	s_add_u32 s2, s11, s12
	s_addc_u32 s3, s6, s5
	s_add_i32 s85, s80, 0x2000
	s_mov_b32 m0, s85
	s_nop 0
	global_load_lds_dwordx4 v102, s[2:3]
	s_add_u32 s2, s7, s12
	s_addc_u32 s3, s8, s5
	s_add_i32 s91, s80, 0x8000
	s_mov_b32 m0, s91
	s_nop 0
	global_load_lds_dwordx4 v94, s[2:3]
	s_mov_b64 s[2:3], -1
	s_and_b64 vcc, exec, s[38:39]
	s_cbranch_vccz .LBB0_637
	s_waitcnt vmcnt(2)
	s_mov_b64 s[2:3], 0
.LBB0_637:
	s_andn2_b64 vcc, exec, s[2:3]
	s_lshl_b32 s88, s4, 6
	s_cbranch_vccnz .LBB0_639
	s_lshl_b64 s[2:3], s[44:45], 11
	s_add_u32 s2, s9, s2
	s_addc_u32 s3, s10, s3
	v_readlane_b32 s5, v254, 59
	s_mov_b32 m0, s5
	s_nop 0
	global_load_lds_dword v99, s[2:3]
	s_waitcnt vmcnt(3)

; #define ATT_ISSUE(st_, sl) do { _Pragma("unroll") for (int sb_ = 0; sb_ < NSUB; ++sb_) ATT_DMA(ATT_TILE((st_) * NSUB + sb_), sl, sb_); } while (0)
; template <int MODE, int DQK, int DV>
; __device__ __forceinline__ void attn_pass(LAS unsigned char* lds, const Tens& T, size_t rowbase, int q0, f32x16 (&o)[DV / 32], float& l_out, const int wave, QPre* qp = nullptr) {
;     ...
;         { constexpr int sl2 = (sl + NRING - 1) % NRING; if (st + NRING - 1 < nst) ATT_ISSUE(st + NRING - 1, sl2); }
.LBB0_640:
	s_add_i32 s1, s89, -2
	s_cmp_ge_u32 s1, s84
	s_cselect_b64 s[74:75], -1, 0
	s_cmp_lt_u32 s1, s84
	s_cselect_b64 s[76:77], -1, 0
	s_and_b64 vcc, exec, s[74:75]
	s_cbranch_vccnz .LBB0_643
	s_add_u32 s1, s86, s72
	s_addc_u32 s7, s87, s73
	s_add_u32 s6, s1, 0x70000
	s_addc_u32 s7, s7, 0
	s_add_i32 s1, s80, 0x4000
	s_mov_b32 m0, s1
	s_nop 0
	global_load_lds_dwordx4 v102, s[6:7]
	s_add_u32 s1, s47, s72
	s_addc_u32 s7, s92, s73
	v_readlane_b32 s8, v254, 26
	s_add_u32 s6, s1, 0x70000
	v_readlane_b32 s9, v254, 27
	s_addc_u32 s7, s7, 0
	s_add_i32 s1, s80, 0xa000
	s_and_b64 vcc, exec, s[8:9]
	s_mov_b32 m0, s1
	s_nop 0
	global_load_lds_dwordx4 v94, s[6:7]
	s_cbranch_vccnz .LBB0_643
	s_add_u32 s6, s70, 0x1000
	s_addc_u32 s7, s71, 0
	s_mov_b32 m0, s49
	s_nop 0
	global_load_lds_dword v99, s[6:7]

; #define ATT_ISSUE(st_, sl) do { _Pragma("unroll") for (int sb_ = 0; sb_ < NSUB; ++sb_) ATT_DMA(ATT_TILE((st_) * NSUB + sb_), sl, sb_); } while (0)
; template <int MODE, int DQK, int DV>
; __device__ __forceinline__ void attn_pass(LAS unsigned char* lds, const Tens& T, size_t rowbase, int q0, f32x16 (&o)[DV / 32], float& l_out, const int wave, QPre* qp = nullptr) {
;     ...
;         { constexpr int sl2 = (sl + NRING - 1) % NRING; if (st + NRING - 1 < nst) ATT_ISSUE(st + NRING - 1, sl2); }
;     ...
;         if (MODE == AM_FOX) {
;             int alld = 1;
; #pragma unroll
;             for (int w_ = 0; w_ < 8; ++w_) alld &= dflag[(st & 1) * 8 + w_];
;             if (alld) return false;
.LBB0_654:
	s_and_b32 s1, s44, 8
	s_lshl_b32 s96, s1, 2
	s_add_i32 s1, s96, 0
	s_add_i32 s1, s1, 0x1fc10
	s_waitcnt lgkmcnt(0)
	s_barrier
	v_mov_b32_e32 v32, s1
	ds_read_b32 v33, v32
	ds_read_b32 v34, v32 offset:4
	s_waitcnt lgkmcnt(0)
	v_and_b32_e32 v33, v33, v34
	ds_read_b32 v34, v32 offset:8
	s_waitcnt lgkmcnt(0)
	v_and_b32_e32 v33, v33, v34
	ds_read_b32 v34, v32 offset:12
	s_waitcnt lgkmcnt(0)
	v_and_b32_e32 v33, v33, v34
	ds_read_b32 v34, v32 offset:16
	s_waitcnt lgkmcnt(0)
	v_and_b32_e32 v33, v33, v34
	ds_read_b32 v34, v32 offset:20
	s_waitcnt lgkmcnt(0)
	v_and_b32_e32 v33, v33, v34
	ds_read_b32 v34, v32 offset:24
	ds_read_b32 v32, v32 offset:28
	s_waitcnt lgkmcnt(1)
	v_and_b32_e32 v33, v33, v34
	s_waitcnt lgkmcnt(0)
	v_and_b32_e32 v32, v33, v32
	v_and_b32_e32 v32, 1, v32
	v_cmp_eq_u32_e32 vcc, 1, v32
	s_cbranch_vccnz .LBB0_688
	s_add_i32 s6, s89, -3
	s_cmp_lt_u32 s6, s84
	s_cbranch_scc0 .LBB0_688
	s_add_i32 s6, s89, -1
	s_cmp_ge_u32 s6, s84
	s_cselect_b64 s[76:77], -1, 0
	s_cmp_lt_u32 s6, s84
	s_cselect_b64 s[78:79], -1, 0
	s_and_b64 vcc, exec, s[76:77]
	s_cbranch_vccnz .LBB0_659
	s_add_u32 s6, s86, s72
	s_addc_u32 s7, s87, s73
	s_mov_b32 m0, s80
	s_nop 0
	global_load_lds_dwordx4 v102, s[6:7]
	s_add_u32 s6, s47, s72
	v_readlane_b32 s8, v254, 26
	v_readlane_b32 s9, v254, 27
	s_addc_u32 s7, s92, s73
	s_and_b64 vcc, exec, s[8:9]
	s_mov_b32 m0, s81
	s_nop 0
	global_load_lds_dwordx4 v94, s[6:7]
	s_cbranch_vccnz .LBB0_659
	s_add_u32 s6, s70, 0x800
	s_addc_u32 s7, s71, 0
	v_readlane_b32 s9, v254, 57
	s_mov_b32 m0, s9
	s_nop 0
	global_load_lds_dword v99, s[6:7]

; #define ATT_ISSUE(st_, sl) do { _Pragma("unroll") for (int sb_ = 0; sb_ < NSUB; ++sb_) ATT_DMA(ATT_TILE((st_) * NSUB + sb_), sl, sb_); } while (0)
; template <int MODE, int DQK, int DV>
; __device__ __forceinline__ void attn_pass(LAS unsigned char* lds, const Tens& T, size_t rowbase, int q0, f32x16 (&o)[DV / 32], float& l_out, const int wave, QPre* qp = nullptr) {
;     ...
;         { constexpr int sl2 = (sl + NRING - 1) % NRING; if (st + NRING - 1 < nst) ATT_ISSUE(st + NRING - 1, sl2); }
;     ...
;         if (MODE == AM_FOX) {
;             int alld = 1;
; #pragma unroll
;             for (int w_ = 0; w_ < 8; ++w_) alld &= dflag[(st & 1) * 8 + w_];
;             if (alld) return false;
.LBB0_674:
	s_add_i32 s6, s44, 8
	s_and_b32 s6, s6, 8
	s_lshl_b32 s6, s6, 2
	s_add_i32 s6, s6, 0
	s_add_i32 s6, s6, 0x1fc10
	s_waitcnt lgkmcnt(0)
	s_barrier
	v_mov_b32_e32 v32, s6
	ds_read_b32 v33, v32
	ds_read_b32 v34, v32 offset:4
	s_waitcnt lgkmcnt(0)
	v_and_b32_e32 v33, v33, v34
	ds_read_b32 v34, v32 offset:8
	s_waitcnt lgkmcnt(0)
	v_and_b32_e32 v33, v33, v34
	ds_read_b32 v34, v32 offset:12
	s_waitcnt lgkmcnt(0)
	v_and_b32_e32 v33, v33, v34
	ds_read_b32 v34, v32 offset:16
	s_waitcnt lgkmcnt(0)
	v_and_b32_e32 v33, v33, v34
	ds_read_b32 v34, v32 offset:20
	s_waitcnt lgkmcnt(0)
	v_and_b32_e32 v33, v33, v34
	ds_read_b32 v34, v32 offset:24
	ds_read_b32 v32, v32 offset:28
	s_waitcnt lgkmcnt(1)
	v_and_b32_e32 v33, v33, v34
	s_waitcnt lgkmcnt(0)
	v_and_b32_e32 v32, v33, v32
	v_and_b32_e32 v32, 1, v32
	v_cmp_eq_u32_e32 vcc, 1, v32
	s_or_b64 s[6:7], s[74:75], vcc
	s_and_b64 vcc, exec, s[6:7]
	s_cbranch_vccnz .LBB0_688
	s_cmp_ge_u32 s89, s84
	s_cselect_b64 s[74:75], -1, 0
	s_and_b64 vcc, exec, s[74:75]
	s_cbranch_vccnz .LBB0_678
	s_add_u32 s6, s86, s72
	s_addc_u32 s7, s87, s73
	s_add_u32 s6, s6, 0xfff90000
	s_addc_u32 s7, s7, -1
	s_mov_b32 m0, s85
	s_nop 0
	global_load_lds_dwordx4 v102, s[6:7]
	s_add_u32 s6, s47, s72
	s_addc_u32 s7, s92, s73
	v_readlane_b32 s8, v254, 26
	s_add_u32 s6, s6, 0xfff90000
	v_readlane_b32 s9, v254, 27
	s_addc_u32 s7, s7, -1
	s_and_b64 vcc, exec, s[8:9]
	s_mov_b32 m0, s91
	s_nop 0
	global_load_lds_dwordx4 v94, s[6:7]
	s_cbranch_vccnz .LBB0_678
	v_readlane_b32 s7, v254, 59
	s_mov_b32 m0, s7
	s_nop 0
	global_load_lds_dword v99, s[70:71]

; template <int MODE, int DQK, int DV>
; __device__ __forceinline__ void attn_pass(LAS unsigned char* lds, const Tens& T, size_t rowbase, int q0, f32x16 (&o)[DV / 32], float& l_out, const int wave, QPre* qp = nullptr) {
;     ...
;         const bf16* qp = T.Q + (rowbase + tq) * (size_t)T.ldq + 8 * h;
; #pragma unroll
;         for (int s = 0; s < NSTEP; ++s) qf[s] = *(const bf16x8*)(qp + 16 * s);
;     }
;     {
;         f32x4 c0 = {1.f, 1.f, 1.f, 1.f}, c1 = c0, s0 = {0.f, 0.f, 0.f, 0.f}, s1 = s0;
;         if (MODE == AM_MLA) {
;             c0 = *(const f32x4*)(T.rcos + tq * 16 + 8 * h); c1 = *(const f32x4*)(T.rcos + tq * 16 + 8 * h + 4);
;             s0 = *(const f32x4*)(T.rsin + tq * 16 + 8 * h); s1 = *(const f32x4*)(T.rsin + tq * 16 + 8 * h + 4);
;         }
; #pragma unroll
;         for (int s = 0; s < NSTEP; ++s) {
;             if (MODE == AM_MLA && s == NSTEP - 1) continue;
;             bf16x8 a = qf[s];
;             if (MODE == AM_MLA && s == NSTEP - 2) {
;                 bf16x8 b2 = qf[NSTEP - 1];
; #pragma unroll
;                 for (int j = 0; j < 8; ++j) {
;                     const float x1 = __uint_as_float(((unsigned)(unsigned short)a[j]) << 16), x2 = __uint_as_float(((unsigned)(unsigned short)b2[j]) << 16);
;                     const float cs = j < 4 ? c0[j & 3] : c1[j & 3], sn = j < 4 ? s0[j & 3] : s1[j & 3];
; template <int PH>
; __device__ __forceinline__ void mk_body(const Args& a) {
;     ...
;             const int u = att::next_unit_pre(qp, ctl + CW_Q + 1 * 512, 256, lds, att::OFF_MISC, wave);
;             if (u < 0) break;
;             const int b = u >> 8, h = (u >> 5) & 7, qb = 31 - (u & 31);
;             { const int t_ = wave * 64 + lane_id_v();
;               if (t_ <= 128) ((LAS float*)(lds + att::OFF_LUT))[t_] = (t_ < 128) ? (t5[bucket_tab[t_] * 8 + h] - t5[31 * 8 + h]) * att::LOG2E : 0.f;
;               if (t_ >= 192 && t_ < 256) { const int e_ = (t_ - 192) >> 2, c_ = t_ & 3; ((LAS float*)(lds + att::OFF_LUT + 768))[t_ - 192] = ((e_ >> c_) & 1) ? 0.f : -INFINITY; } }
;             att::Tens T{};
;             T.Q = y0 + Y0_DQ + h * 64; T.ldq = Y0P; T.K = y0 + Y0_DK + h * 64; T.ldk = Y0P; T.V = y0 + Y0_DV + h * 64; T.ldv = Y0P;
;             T.mask = maskg; T.scale2 = 0.125f * att::LOG2E;
;             att::f32x16 o[2]; float l;
;             att::attn_pass<att::AM_DSA, 64, 64>(lds, T, (size_t)b * S, qb * 256, o, l, wave, &qp);
.LBB0_1618:
	s_lshr_b32 s12, s8, 8
	s_lshl_b32 s0, s0, 8
	s_add_u32 s16, s6, s0
	s_addc_u32 s17, s7, 0
	s_lshl_b32 s81, s1, 6
	s_lshl_b32 s0, s1, 7
	s_add_u32 s10, s92, s0
	s_addc_u32 s11, s40, 0
	s_add_u32 s1, s41, s0
	s_addc_u32 s2, s44, 0
	s_add_u32 s3, s45, s0
	s_addc_u32 s4, s46, 0
	s_not_b32 s0, s8
	s_lshl_b32 s0, s0, 8
	s_and_b32 s82, s0, 0x1f00
	v_mbcnt_lo_u32_b32 v28, -1, 0
	v_mbcnt_hi_u32_b32 v28, -1, v28
	s_add_i32 s83, s82, s49
	v_and_b32_e32 v29, 31, v28
	s_lshl_b64 s[18:19], s[12:13], 13
	v_or_b32_e32 v0, s83, v29
	v_mov_b32_e32 v1, v66
	v_lshl_add_u64 v[0:1], s[18:19], 0, v[0:1]
	v_mov_b64_e32 v[2:3], s[10:11]
	s_movk_i32 s0, 0x1c00
	v_bfe_u32 v30, v28, 5, 1
	v_mad_u64_u32 v[2:3], s[8:9], v0, s0, v[2:3]
	v_mad_u32_u24 v3, v1, s0, v3
	v_lshlrev_b32_e32 v0, 4, v30
	v_mov_b32_e32 v1, v66
	v_lshl_add_u64 v[12:13], v[2:3], 0, v[0:1]
	global_load_dwordx4 v[0:3], v[12:13], off
	global_load_dwordx4 v[4:7], v[12:13], off offset:32
	global_load_dwordx4 v[8:11], v[12:13], off offset:64
	s_movk_i32 s5, 0xe00
	global_load_dwordx4 v[12:15], v[12:13], off offset:96
	s_add_i32 s0, s82, 0x100
	s_lshl_b64 s[8:9], s[12:13], 23
	s_mul_i32 s11, s12, 0x3800000
	s_mul_hi_u32 s10, s12, 0x3800000
	v_and_b32_e32 v31, 63, v28
	v_lshlrev_b32_e32 v106, 2, v30
	v_lshlrev_b32_e32 v105, 3, v29
	s_mov_b32 s84, 4
	v_mov_b32_e32 v65, v66
	v_mov_b32_e32 v67, v66
	v_mov_b32_e32 v70, v66
	v_mov_b32_e32 v71, v66
	v_or_b32_e32 v107, 8, v106
	v_or_b32_e32 v108, 16, v106
	v_or_b32_e32 v109, 24, v106
	v_mov_b32_e32 v111, 0
	v_mov_b32_e32 v112, 0xc2800000
	v_mov_b32_e32 v103, 0
	s_mov_b64 s[26:27], 0
	s_waitcnt vmcnt(0)
	v_and_b32_e32 v17, 0xffff0000, v0
	v_lshlrev_b32_e32 v16, 16, v0
	v_and_b32_e32 v19, 0xffff0000, v1
	v_lshlrev_b32_e32 v18, 16, v1
	v_and_b32_e32 v1, 0xffff0000, v2
	v_lshlrev_b32_e32 v0, 16, v2
	v_and_b32_e32 v21, 0xffff0000, v3
	v_lshlrev_b32_e32 v20, 16, v3
	v_and_b32_e32 v3, 0xffff0000, v4
	v_lshlrev_b32_e32 v2, 16, v4
	v_and_b32_e32 v25, 0xffff0000, v7
	v_lshlrev_b32_e32 v24, 16, v7
	v_pk_mul_f32 v[20:21], v[20:21], s[14:15] op_sel_hi:[1,0]
	v_pk_mul_f32 v[2:3], v[2:3], s[14:15] op_sel_hi:[1,0]
	v_and_b32_e32 v23, 0xffff0000, v5
	v_lshlrev_b32_e32 v22, 16, v5
	v_and_b32_e32 v5, 0xffff0000, v6
	v_lshlrev_b32_e32 v4, 16, v6
	v_and_b32_e32 v7, 0xffff0000, v8
	v_lshlrev_b32_e32 v6, 16, v8
	v_and_b32_e32 v27, 0xffff0000, v9
	v_lshlrev_b32_e32 v26, 16, v9
	v_and_b32_e32 v9, 0xffff0000, v10
	v_lshlrev_b32_e32 v8, 16, v10
	v_pk_mul_f32 v[16:17], v[16:17], s[14:15] op_sel_hi:[1,0]
	v_pk_mul_f32 v[24:25], v[24:25], s[14:15] op_sel_hi:[1,0]
	v_bfe_u32 v10, v21, 16, 1
	v_bfe_u32 v32, v20, 16, 1
	v_bfe_u32 v45, v3, 16, 1
	v_bfe_u32 v46, v2, 16, 1
	v_pk_mul_f32 v[18:19], v[18:19], s[14:15] op_sel_hi:[1,0]
	v_pk_mul_f32 v[0:1], v[0:1], s[14:15] op_sel_hi:[1,0]
	v_pk_mul_f32 v[4:5], v[4:5], s[14:15] op_sel_hi:[1,0]
	v_pk_mul_f32 v[6:7], v[6:7], s[14:15] op_sel_hi:[1,0]
	v_bfe_u32 v38, v16, 16, 1
	v_bfe_u32 v39, v25, 16, 1
	v_add3_u32 v20, v20, v32, s76
	v_add3_u32 v10, v21, v10, s76
	v_add3_u32 v21, v2, v46, s76
	v_add3_u32 v32, v3, v45, s76
	v_and_b32_e32 v3, 0xffff0000, v11
	v_lshlrev_b32_e32 v2, 16, v11
	v_pk_mul_f32 v[26:27], v[26:27], s[14:15] op_sel_hi:[1,0]
	v_bfe_u32 v33, v1, 16, 1
	v_bfe_u32 v34, v0, 16, 1
	v_bfe_u32 v35, v19, 16, 1
	v_bfe_u32 v36, v18, 16, 1
	v_bfe_u32 v37, v17, 16, 1
	v_bfe_u32 v41, v5, 16, 1
	v_bfe_u32 v42, v4, 16, 1
	v_add3_u32 v16, v16, v38, s76
	v_add3_u32 v25, v25, v39, s76
	v_pk_mul_f32 v[2:3], v[2:3], s[14:15] op_sel_hi:[1,0]
	v_bfe_u32 v38, v7, 16, 1
	v_bfe_u32 v39, v6, 16, 1
	v_add3_u32 v17, v17, v37, s76
	v_add3_u32 v18, v18, v36, s76
	v_add3_u32 v19, v19, v35, s76
	v_add3_u32 v34, v0, v34, s76
	v_add3_u32 v33, v1, v33, s76
	v_add3_u32 v35, v4, v42, s76
	v_add3_u32 v36, v5, v41, s76
	v_pk_mul_f32 v[0:1], v[8:9], s[14:15] op_sel_hi:[1,0]
	v_bfe_u32 v4, v3, 16, 1
	v_bfe_u32 v5, v2, 16, 1
	v_bfe_u32 v11, v27, 16, 1
	v_bfe_u32 v37, v26, 16, 1
	v_add3_u32 v39, v6, v39, s76
	v_add3_u32 v38, v7, v38, s76
	v_and_b32_e32 v7, 0xffff0000, v15
	v_lshlrev_b32_e32 v6, 16, v15
	v_bfe_u32 v8, v1, 16, 1
	v_bfe_u32 v9, v0, 16, 1
	v_add3_u32 v26, v26, v37, s76
	v_add3_u32 v11, v27, v11, s76
	v_add3_u32 v27, v2, v5, s76
	v_add3_u32 v37, v3, v4, s76
	v_and_b32_e32 v3, 0xffff0000, v13
	v_lshlrev_b32_e32 v2, 16, v13
	v_and_b32_e32 v5, 0xffff0000, v14
	v_lshlrev_b32_e32 v4, 16, v14
	v_pk_mul_f32 v[6:7], v[6:7], s[14:15] op_sel_hi:[1,0]
	v_bfe_u32 v40, v24, 16, 1
	v_add3_u32 v9, v0, v9, s76
	v_add3_u32 v8, v1, v8, s76
	v_and_b32_e32 v1, 0xffff0000, v12
	v_lshlrev_b32_e32 v0, 16, v12
	v_pk_mul_f32 v[2:3], v[2:3], s[14:15] op_sel_hi:[1,0]
	v_pk_mul_f32 v[4:5], v[4:5], s[14:15] op_sel_hi:[1,0]
	v_bfe_u32 v12, v7, 16, 1
	v_add3_u32 v24, v24, v40, s76
	v_bfe_u32 v13, v6, 16, 1
	v_bfe_u32 v15, v4, 16, 1
	v_bfe_u32 v40, v3, 16, 1
	v_add3_u32 v7, v7, v12, s76
	v_bfe_u32 v12, v28, 3, 3
	v_bfe_u32 v14, v5, 16, 1
	v_add3_u32 v3, v3, v40, s76
	v_add3_u32 v4, v4, v15, s76
	v_add3_u32 v6, v6, v13, s76
	v_or_b32_e32 v13, s64, v12
	v_lshrrev_b32_e32 v15, 4, v28
	v_lshrrev_b32_e32 v40, 2, v28
	v_add3_u32 v5, v5, v14, s76
; #define LAS __attribute__((address_space(3)))
; #define ATT_ISSUE(st_, sl) do { _Pragma("unroll") for (int sb_ = 0; sb_ < NSUB; ++sb_) ATT_DMA(ATT_TILE((st_) * NSUB + sb_), sl, sb_); } while (0)
; #define ATT_BAR() asm volatile("s_waitcnt lgkmcnt(0)\n\ts_barrier" ::: "memory")
; template <int MODE, int DQK, int DV>
; __device__ __forceinline__ void attn_pass(LAS unsigned char* lds, const Tens& T, size_t rowbase, int q0, f32x16 (&o)[DV / 32], float& l_out, const int wave, QPre* qp = nullptr) {
;     ...
;     const int nvm = 1 + ((DQK == 96 && wave < 4) ? 1 : 0) + DV / 64 + ((MODE == AM_FOX && wave == 0) ? 1 : 0) + ((MODE == AM_DSA) ? 1 : 0);
;     ...
;     const unsigned koff = (unsigned)(r * 128), kswz = (unsigned)((r >> 1) & 7);
;     const unsigned roff = (unsigned)(8192 + r * 64), rswz = (unsigned)((r >> 2) & 3);
;     const int g16 = lane >> 4, qq = (lane & 15) >> 2, pp = lane & 3;
;     const int vsw = (DV == 64) ? ((qq >> 1) & 1) : qq;
;     const unsigned voff = (unsigned)((4 * (g16 >> 1) + qq) * VROW + (16 * (g16 & 1) + 4 * pp) * 2);
;     const LAS unsigned char* kfa[NSTEP]; const LAS unsigned char* vfa[NDB];
; #pragma unroll
;     for (int s = 0; s < NSTEP; ++s) {
;         kfa[s] = (s < 4) ? lds + OFF_K + koff + (((unsigned)(2 * s + h) ^ kswz) * 16) : lds + OFF_K + roff + (((unsigned)(2 * (s - 4) + h) ^ rswz) * 16);
;         asm volatile("" : "+v"(kfa[s]));
;     }
; #pragma unroll
;     for (int db = 0; db < NDB; ++db) { vfa[db] = lds + OFF_V + voff + (unsigned)((db ^ vsw) * 64); asm volatile("" : "+v"(vfa[db])); }
;     float m = -64.0f, l = 0.f;
;     bf16x8 kone = {0, 0, 0, 0, 0, 0, 0, 0}, qm = kone;
;     if (MODE == AM_DSA) { if (h == 0) { kone[0] = (short)0x3F80; kone[1] = (short)0x3F80; kone[2] = (short)0x3F80; } qm = split3_bf16(64.0f, h); }
;     f32x16 negm;
; #pragma unroll
;     for (int rg = 0; rg < 16; ++rg) negm[rg] = 64.0f;
; #pragma unroll
;     for (int i = 0; i < NDB; ++i) o[i] = f32x16{};
;     const int jlast = (q0 + wave * 32) / 64;
;     constexpr bool DESC = (MODE == AM_FOX);
;     ...
;     bool wdone = false;
;     volatile LAS int* dflag = (volatile LAS int*)(lds + OFF_MISC + 16);
;     const int nst = ntile / NSUB;
;     ATT_ISSUE(0, 0);
;     if (NRING == 3) ATT_ISSUE(1, 1);
;     if (NRING == 3) ATT_WAIT_PREV(); else asm volatile("s_waitcnt vmcnt(0)" ::: "memory");
;     ATT_BAR();
	v_lshrrev_b32_e32 v14, 1, v13
	v_xor_b32_e32 v15, v40, v15
	v_bfe_u32 v41, v2, 16, 1
	v_xor_b32_e32 v14, v14, v28
	v_lshlrev_b32_e32 v15, 5, v15
	v_lshlrev_b32_e32 v40, 3, v28
	v_mul_lo_u32 v13, v13, s5
	s_lshl_b32 s5, s82, 3
	v_pk_mul_f32 v[0:1], v[0:1], s[14:15] op_sel_hi:[1,0]
	v_add3_u32 v2, v2, v41, s76
	v_lshlrev_b32_e32 v14, 3, v14
	v_and_b32_e32 v15, 32, v15
	v_and_b32_e32 v41, 24, v40
	s_add_u32 s20, s3, s11
	v_bfe_u32 v42, v1, 16, 1
	v_and_or_b32 v14, v14, 56, v13
	v_or3_b32 v13, v41, v15, v13
	s_addc_u32 s21, s4, s10
	v_add3_u32 v1, v1, v42, s76
	v_lshlrev_b32_e32 v95, 1, v13
	v_lshlrev_b32_e32 v13, 2, v31
	v_lshrrev_b32_e32 v15, 1, v28
	v_bfe_u32 v41, v28, 1, 3
	v_bfe_u32 v42, v28, 2, 2
	v_and_b32_e32 v28, 16, v28
	s_add_u32 s22, s1, s11
	v_and_or_b32 v12, v12, 4, v42
	v_and_or_b32 v28, v13, 12, v28
	v_lshl_add_u32 v42, v29, 7, 0
	v_bitop3_b32 v15, v30, v15, 7 bitop3:0x78
	s_addc_u32 s23, s2, s10
	v_lshl_add_u32 v96, v15, 4, v42
	v_bitop3_b32 v15, v30, v41, 2 bitop3:0x36
	v_or_b32_e32 v100, s65, v13
	v_lshlrev_b32_e32 v12, 7, v12
	v_lshlrev_b32_e32 v13, 1, v28
	s_add_u32 s1, s47, s8
	v_lshl_add_u32 v97, v15, 4, v42
	v_bitop3_b32 v15, v30, v41, 4 bitop3:0x36
	v_add3_u32 v12, 0, v12, v13
	v_and_b32_e32 v13, 64, v40
	s_mov_b32 s3, 0xc000
	s_addc_u32 s2, s48, s9
	v_lshl_add_u32 v98, v15, 4, v42
	v_bitop3_b32 v15, v30, v41, 6 bitop3:0x36
	v_add3_u32 v101, v12, v13, s3
	v_bitop3_b32 v13, v40, 64, v40 bitop3:0xc
	s_add_u32 s24, s1, s5
	v_lshl_add_u32 v99, v15, 4, v42
	v_add3_u32 v102, v12, v13, s3
	s_addc_u32 s25, s2, 0
	s_add_i32 s85, s66, 0
	v_lshlrev_b32_e32 v104, 1, v14
	s_lshr_b32 s12, s83, 6
	s_mov_b32 m0, s85
	s_nop 0
	global_load_lds_dwordx4 v104, s[22:23]
	s_add_i32 s88, s85, 0xc000
	s_mov_b32 m0, s88
	s_nop 0
	global_load_lds_dwordx4 v95, s[20:21]
	s_add_u32 s2, s22, 0x70000
	s_mov_b32 m0, s67
	s_nop 0
	global_load_lds_dword v100, s[24:25]
	s_addc_u32 s3, s23, 0
	s_add_i32 s89, s85, 0x2000
	s_mov_b32 m0, s89
	s_nop 0
	global_load_lds_dwordx4 v104, s[2:3]
	s_add_u32 s2, s20, 0x70000
	s_addc_u32 s3, s21, 0
	s_add_i32 s91, s85, 0xe000
	s_mov_b32 m0, s91
	s_nop 0
	global_load_lds_dwordx4 v95, s[2:3]
	s_add_u32 s2, s24, 0x10000
	s_addc_u32 s3, s25, 0
	s_mov_b32 m0, s68
	s_nop 0
	global_load_lds_dword v100, s[2:3]
	s_add_u32 s2, s22, 0xe0000
	s_addc_u32 s3, s23, 0
	s_add_i32 s93, s85, 0x4000
	s_mov_b32 m0, s93
	s_nop 0
	global_load_lds_dwordx4 v104, s[2:3]
	s_add_u32 s2, s20, 0xe0000
	s_addc_u32 s3, s21, 0
	s_add_i32 s94, s85, 0x10000
	s_mov_b32 m0, s94
	s_nop 0
	global_load_lds_dwordx4 v95, s[2:3]
	s_add_u32 s2, s24, 0x20000
	s_addc_u32 s3, s25, 0
	s_mov_b32 m0, s69
	s_nop 0
	global_load_lds_dword v100, s[2:3]
	s_add_u32 s2, s22, 0x150000
	s_addc_u32 s3, s23, 0
	s_add_i32 s95, s85, 0x6000
	s_mov_b32 m0, s95
	s_nop 0
	global_load_lds_dwordx4 v104, s[2:3]
	s_add_u32 s2, s20, 0x150000
	s_addc_u32 s3, s21, 0
	s_add_i32 s96, s85, 0x12000
	v_pk_mul_f32 v[22:23], v[22:23], s[14:15] op_sel_hi:[1,0]
	s_mov_b32 m0, s96
	s_nop 0
	global_load_lds_dwordx4 v95, s[2:3]
	s_add_u32 s2, s24, 0x30000
	v_bfe_u32 v43, v23, 16, 1
	s_addc_u32 s3, s25, 0
	s_mov_b32 m0, s70
	s_nop 0
	global_load_lds_dword v100, s[2:3]
	v_add3_u32 v23, v23, v43, s76
	v_bfe_u32 v43, v0, 16, 1
	s_lshr_b32 s97, s0, 7
	s_add_i32 s8, s83, 0xffffff01
	s_add_i32 s1, s73, s82
	v_bfe_u32 v44, v22, 16, 1
	v_add3_u32 v0, v0, v43, s76
	s_waitcnt vmcnt(6)
	s_add_u32 s24, s24, 0x90000
	v_add3_u32 v22, v22, v44, s76
	s_waitcnt lgkmcnt(0)
	s_barrier
	v_or_b32_e32 v12, s90, v31
	v_perm_b32 v72, v17, v16, s78
	v_perm_b32 v84, v1, v0, s78
	v_add_u32_e32 v0, s1, v29
	s_addc_u32 s25, s25, 0
	s_lshr_b32 s0, s0, 6
	v_mov_b32_e32 v16, v66
	v_mov_b32_e32 v17, v66
	v_cmp_gt_u32_e64 s[2:3], 32, v31
	v_cmp_ne_u32_e64 s[4:5], 0, v12
	v_perm_b32 v75, v10, v20, s78
	v_perm_b32 v73, v19, v18, s78
	v_perm_b32 v79, v25, v24, s78
	v_perm_b32 v77, v23, v22, s78
	v_perm_b32 v76, v32, v21, s78
	v_perm_b32 v83, v37, v27, s78
	v_perm_b32 v82, v8, v9, s78
	v_perm_b32 v81, v11, v26, s78
	v_perm_b32 v87, v7, v6, s78
	v_perm_b32 v86, v5, v4, s78
	v_perm_b32 v85, v3, v2, s78
	v_sub_u32_e32 v110, v0, v106
	s_mul_i32 s0, s0, 0x70000
	v_mov_b32_e32 v18, v66
	v_mov_b32_e32 v19, v66
	v_mov_b32_e32 v20, v66
	v_mov_b32_e32 v21, v66
	v_mov_b32_e32 v22, v66
	v_mov_b32_e32 v23, v66
	v_mov_b32_e32 v24, v66
	v_mov_b32_e32 v25, v66
	v_mov_b32_e32 v26, v66
	v_mov_b32_e32 v27, v66
	v_mov_b32_e32 v28, v66
	v_mov_b32_e32 v29, v66
	v_mov_b32_e32 v30, v66
	v_mov_b32_e32 v31, v66
	v_mov_b64_e32 v[0:1], v[16:17]
	v_cndmask_b32_e64 v64, 0, v90, s[2:3]
	s_mov_b32 s10, 0
	v_cndmask_b32_e64 v69, 0, v91, s[2:3]
	v_cndmask_b32_e64 v68, 0, v92, s[2:3]
	v_perm_b32 v74, v33, v34, s78
	v_perm_b32 v78, v36, v35, s78
	v_perm_b32 v80, v38, v39, s78
	s_add_u32 s9, s0, 0xffd60000
	s_add_u32 s75, s0, 0xffe40000
	s_add_u32 s77, s0, 0xffc80000
	s_mov_b32 s11, 0
	v_mov_b64_e32 v[2:3], v[18:19]
	v_mov_b64_e32 v[4:5], v[20:21]
	v_mov_b64_e32 v[6:7], v[22:23]
	v_mov_b64_e32 v[8:9], v[24:25]
	v_mov_b64_e32 v[10:11], v[26:27]
	v_mov_b64_e32 v[12:13], v[28:29]
	v_mov_b64_e32 v[14:15], v[30:31]
	s_branch .LBB0_1621

; #define ATT_ISSUE(st_, sl) do { _Pragma("unroll") for (int sb_ = 0; sb_ < NSUB; ++sb_) ATT_DMA(ATT_TILE((st_) * NSUB + sb_), sl, sb_); } while (0)
; template <int MODE, int DQK, int DV>
; __device__ __forceinline__ void attn_pass(LAS unsigned char* lds, const Tens& T, size_t rowbase, int q0, f32x16 (&o)[DV / 32], float& l_out, const int wave, QPre* qp = nullptr) {
;     ...
;         { constexpr int sl2 = (sl + NRING - 1) % NRING; if (st + NRING - 1 < nst) ATT_ISSUE(st + NRING - 1, sl2); }
.LBB0_1621:
	s_add_i32 s0, s84, -2
	s_cmp_lt_u32 s0, s97
	s_cselect_b64 s[28:29], -1, 0
	s_cmp_ge_u32 s0, s97
	s_cselect_b64 s[30:31], -1, 0
	s_and_b64 vcc, exec, s[30:31]
	s_cbranch_vccnz .LBB0_1623
	s_add_u32 s15, s22, s26
	s_addc_u32 s33, s23, s27
	s_add_u32 s0, s15, 0x1c0000
	s_addc_u32 s1, s33, 0
	s_add_i32 s34, s85, 0x8000
	s_mov_b32 m0, s34
	s_nop 0
	global_load_lds_dwordx4 v104, s[0:1]
	s_add_u32 s34, s20, s26
	s_addc_u32 s35, s21, s27
	s_add_u32 s0, s34, 0x1c0000
	s_addc_u32 s1, s35, 0
	s_add_i32 s36, s85, 0x14000
	s_mov_b32 m0, s36
	s_nop 0
	global_load_lds_dwordx4 v95, s[0:1]
	s_add_u32 s0, s24, 0xfffb0000
	s_addc_u32 s1, s25, -1
	s_mov_b32 m0, s71
	s_nop 0
	global_load_lds_dword v100, s[0:1]
	s_add_u32 s0, s15, 0x230000
	s_addc_u32 s1, s33, 0
	s_add_i32 s15, s85, 0xa000
	s_mov_b32 m0, s15
	s_nop 0
	global_load_lds_dwordx4 v104, s[0:1]
	s_add_u32 s0, s34, 0x230000
	s_addc_u32 s1, s35, 0
	s_add_i32 s15, s85, 0x16000
	s_mov_b32 m0, s15
	s_nop 0
	global_load_lds_dwordx4 v95, s[0:1]
	s_add_u32 s0, s24, 0xfffc0000
	s_addc_u32 s1, s25, -1
	s_mov_b32 m0, s72
	s_nop 0
	global_load_lds_dword v100, s[0:1]

; #define ATT_ISSUE(st_, sl) do { _Pragma("unroll") for (int sb_ = 0; sb_ < NSUB; ++sb_) ATT_DMA(ATT_TILE((st_) * NSUB + sb_), sl, sb_); } while (0)
; template <int MODE, int DQK, int DV>
; __device__ __forceinline__ void attn_pass(LAS unsigned char* lds, const Tens& T, size_t rowbase, int q0, f32x16 (&o)[DV / 32], float& l_out, const int wave, QPre* qp = nullptr) {
;     ...
;         { constexpr int sl2 = (sl + NRING - 1) % NRING; if (st + NRING - 1 < nst) ATT_ISSUE(st + NRING - 1, sl2); }
.LBB0_1629:
	s_waitcnt lgkmcnt(0)
	s_barrier
	s_add_i32 s0, s84, -3
	s_mov_b64 s[30:31], -1
	s_cmp_ge_u32 s0, s97
	s_nop 3
	v_readfirstlane_b32 s0, v0
	v_readfirstlane_b32 s1, v0
	v_readfirstlane_b32 s33, v0
	s_cbranch_scc1 .LBB0_1619
	s_add_i32 s15, s84, -1
	s_cmp_ge_u32 s15, s97
	s_cselect_b64 s[30:31], -1, 0
	s_and_b64 vcc, exec, s[30:31]
	s_cbranch_vccnz .LBB0_1632
	s_add_u32 s33, s22, s26
	s_addc_u32 s34, s23, s27
	s_add_u32 s0, s33, 0x2a0000
	s_addc_u32 s1, s34, 0
	s_mov_b32 m0, s85
	s_nop 0
	global_load_lds_dwordx4 v104, s[0:1]
	s_add_u32 s35, s20, s26
	s_addc_u32 s36, s21, s27
	s_add_u32 s0, s35, 0x2a0000
	s_addc_u32 s1, s36, 0
	s_mov_b32 m0, s88
	s_nop 0
	global_load_lds_dwordx4 v95, s[0:1]
	s_add_u32 s0, s24, 0xfffd0000
	s_addc_u32 s1, s25, -1
	s_mov_b32 m0, s67
	s_nop 0
	global_load_lds_dword v100, s[0:1]
	s_add_u32 s0, s33, 0x310000
	s_addc_u32 s1, s34, 0
	s_mov_b32 m0, s89
	s_nop 0
	global_load_lds_dwordx4 v104, s[0:1]
	s_add_u32 s0, s35, 0x310000
	s_addc_u32 s1, s36, 0
	s_mov_b32 m0, s91
	s_nop 0
	global_load_lds_dwordx4 v95, s[0:1]
	s_add_u32 s0, s24, 0xfffe0000
	s_addc_u32 s1, s25, -1
	s_mov_b32 m0, s68
	s_nop 0
	global_load_lds_dword v100, s[0:1]

; #define ATT_ISSUE(st_, sl) do { _Pragma("unroll") for (int sb_ = 0; sb_ < NSUB; ++sb_) ATT_DMA(ATT_TILE((st_) * NSUB + sb_), sl, sb_); } while (0)
; template <int MODE, int DQK, int DV>
; __device__ __forceinline__ void attn_pass(LAS unsigned char* lds, const Tens& T, size_t rowbase, int q0, f32x16 (&o)[DV / 32], float& l_out, const int wave, QPre* qp = nullptr) {
;     ...
;         { constexpr int sl2 = (sl + NRING - 1) % NRING; if (st + NRING - 1 < nst) ATT_ISSUE(st + NRING - 1, sl2); }
.LBB0_1638:
	s_waitcnt lgkmcnt(0)
	s_barrier
	s_mov_b64 s[30:31], -1
	s_nop 5
	v_readfirstlane_b32 s0, v0
	v_readfirstlane_b32 s1, v0
	s_andn2_b64 vcc, exec, s[28:29]
	v_readfirstlane_b32 s33, v0
	s_cbranch_vccnz .LBB0_1619
	s_cmp_ge_u32 s84, s97
	s_cselect_b64 s[28:29], -1, 0
	s_and_b64 vcc, exec, s[28:29]
	s_cbranch_vccnz .LBB0_1641
	s_add_u32 s30, s22, s26
	s_addc_u32 s31, s23, s27
	s_add_u32 s0, s30, 0x380000
	s_addc_u32 s1, s31, 0
	s_mov_b32 m0, s93
	s_nop 0
	global_load_lds_dwordx4 v104, s[0:1]
	s_add_u32 s33, s20, s26
	s_addc_u32 s34, s21, s27
	s_add_u32 s0, s33, 0x380000
	s_addc_u32 s1, s34, 0
	s_mov_b32 m0, s94
	s_nop 0
	global_load_lds_dwordx4 v95, s[0:1]
	s_add_u32 s0, s24, 0xffff0000
	s_addc_u32 s1, s25, -1
	s_mov_b32 m0, s69
	s_nop 0
	global_load_lds_dword v100, s[0:1]
	s_add_u32 s0, s30, 0x3f0000
	s_addc_u32 s1, s31, 0
	s_mov_b32 m0, s95
	s_nop 0
	global_load_lds_dwordx4 v104, s[0:1]
	s_add_u32 s0, s33, 0x3f0000
	s_addc_u32 s1, s34, 0
	s_mov_b32 m0, s96
	s_nop 0
	global_load_lds_dwordx4 v95, s[0:1]
	s_mov_b32 m0, s70
	s_nop 0
	global_load_lds_dword v100, s[24:25]

; template <int MODE, int DQK, int DV>
; __device__ __forceinline__ void attn_pass(LAS unsigned char* lds, const Tens& T, size_t rowbase, int q0, f32x16 (&o)[DV / 32], float& l_out, const int wave, QPre* qp = nullptr) {
;     ...
;         const bf16* qp = T.Q + (rowbase + tq) * (size_t)T.ldq + 8 * h;
; #pragma unroll
;         for (int s = 0; s < NSTEP; ++s) qf[s] = *(const bf16x8*)(qp + 16 * s);
;     }
;     {
;         f32x4 c0 = {1.f, 1.f, 1.f, 1.f}, c1 = c0, s0 = {0.f, 0.f, 0.f, 0.f}, s1 = s0;
;         if (MODE == AM_MLA) {
;             c0 = *(const f32x4*)(T.rcos + tq * 16 + 8 * h); c1 = *(const f32x4*)(T.rcos + tq * 16 + 8 * h + 4);
;             s0 = *(const f32x4*)(T.rsin + tq * 16 + 8 * h); s1 = *(const f32x4*)(T.rsin + tq * 16 + 8 * h + 4);
;         }
; #pragma unroll
;         for (int s = 0; s < NSTEP; ++s) {
;             if (MODE == AM_MLA && s == NSTEP - 1) continue;
;             bf16x8 a = qf[s];
;             if (MODE == AM_MLA && s == NSTEP - 2) {
;                 bf16x8 b2 = qf[NSTEP - 1];
; #pragma unroll
;                 for (int j = 0; j < 8; ++j) {
;                     const float x1 = __uint_as_float(((unsigned)(unsigned short)a[j]) << 16), x2 = __uint_as_float(((unsigned)(unsigned short)b2[j]) << 16);
;                     const float cs = j < 4 ? c0[j & 3] : c1[j & 3], sn = j < 4 ? s0[j & 3] : s1[j & 3];
;                     a[j] = (short)f2bf((x1 * cs - x2 * sn) * T.scale2); b2[j] = (short)f2bf((x2 * cs + x1 * sn) * T.scale2);
;                 }
;                 qf[NSTEP - 1] = b2;
;             } else {
; #pragma unroll
;                 for (int j = 0; j < 8; ++j) a[j] = (short)f2bf(__uint_as_float(((unsigned)(unsigned short)a[j]) << 16) * T.scale2);
;             }
;             qf[s] = a;
;         }
;     ...
;     const int nvm = 1 + ((DQK == 96 && wave < 4) ? 1 : 0) + DV / 64 + ((MODE == AM_FOX && wave == 0) ? 1 : 0) + ((MODE == AM_DSA) ? 1 : 0);
;     ...
;     const unsigned koff = (unsigned)(r * 128), kswz = (unsigned)((r >> 1) & 7);
;     const unsigned roff = (unsigned)(8192 + r * 64), rswz = (unsigned)((r >> 2) & 3);
;     const int g16 = lane >> 4, qq = (lane & 15) >> 2, pp = lane & 3;
;     const int vsw = (DV == 64) ? ((qq >> 1) & 1) : qq;
;     const unsigned voff = (unsigned)((4 * (g16 >> 1) + qq) * VROW + (16 * (g16 & 1) + 4 * pp) * 2);
;     const LAS unsigned char* kfa[NSTEP]; const LAS unsigned char* vfa[NDB];
; #pragma unroll
.LBB0_2438:
	s_or_b64 exec, exec, s[4:5]
	v_mbcnt_lo_u32_b32 v1, -1, 0
	v_mbcnt_hi_u32_b32 v1, -1, v1
	s_xor_b64 s[60:61], s[2:3], -1
	v_and_b32_e32 v32, 31, v1
	s_lshl_b32 s0, s34, 7
	v_or_b32_e32 v144, s95, v32
	s_add_u32 s2, s45, s0
	v_lshl_add_u64 v[2:3], s[46:47], 0, v[144:145]
	s_addc_u32 s3, s74, 0
	v_bfe_u32 v33, v1, 5, 1
	v_lshlrev_b64 v[2:3], 12, v[2:3]
	v_lshl_add_u64 v[2:3], s[2:3], 0, v[2:3]
	v_lshlrev_b32_e32 v4, 4, v33
	v_mov_b32_e32 v5, v145
	v_lshl_add_u64 v[14:15], v[2:3], 0, v[4:5]
	global_load_dwordx4 v[2:5], v[14:15], off
	global_load_dwordx4 v[6:9], v[14:15], off offset:32
	global_load_dwordx4 v[10:13], v[14:15], off offset:64
	s_nop 0
	global_load_dwordx4 v[14:17], v[14:15], off offset:96
	s_movk_i32 s1, 0x70
	s_add_u32 s64, s96, s0
	s_addc_u32 s65, s97, 0
	s_add_i32 s92, s81, 0
	s_add_i32 s75, s82, 0
	s_add_i32 s76, s75, 0x8000
	s_add_i32 s77, s75, 0x8400
	v_lshlrev_b32_e32 v163, 2, v33
	v_sub_u32_e32 v164, v144, v163
	v_mov_b32_e32 v165, 0
	v_mov_b32_e32 v166, 0xc2800000
	s_waitcnt vmcnt(3)
	v_and_b32_e32 v19, 0xffff0000, v2
	v_lshlrev_b32_e32 v18, 16, v2
	v_and_b32_e32 v21, 0xffff0000, v3
	v_lshlrev_b32_e32 v20, 16, v3
	v_and_b32_e32 v3, 0xffff0000, v4
	v_lshlrev_b32_e32 v2, 16, v4
	v_and_b32_e32 v23, 0xffff0000, v5
	v_lshlrev_b32_e32 v22, 16, v5
	s_waitcnt vmcnt(2)
	v_and_b32_e32 v5, 0xffff0000, v6
	v_lshlrev_b32_e32 v4, 16, v6
	v_and_b32_e32 v25, 0xffff0000, v7
	v_lshlrev_b32_e32 v24, 16, v7
	v_and_b32_e32 v7, 0xffff0000, v8
	v_lshlrev_b32_e32 v6, 16, v8
	v_and_b32_e32 v27, 0xffff0000, v9
	v_lshlrev_b32_e32 v26, 16, v9
	s_waitcnt vmcnt(1)
	v_and_b32_e32 v9, 0xffff0000, v10
	v_lshlrev_b32_e32 v8, 16, v10
	v_and_b32_e32 v29, 0xffff0000, v11
	v_lshlrev_b32_e32 v28, 16, v11
	v_and_b32_e32 v11, 0xffff0000, v12
	v_lshlrev_b32_e32 v10, 16, v12
	v_and_b32_e32 v31, 0xffff0000, v13
	v_lshlrev_b32_e32 v30, 16, v13
	v_pk_mul_f32 v[12:13], v[18:19], s[44:45] op_sel_hi:[1,0]
	v_pk_mul_f32 v[18:19], v[20:21], s[44:45] op_sel_hi:[1,0]
	v_pk_mul_f32 v[2:3], v[2:3], s[44:45] op_sel_hi:[1,0]
	v_pk_mul_f32 v[20:21], v[22:23], s[44:45] op_sel_hi:[1,0]
	v_pk_mul_f32 v[4:5], v[4:5], s[44:45] op_sel_hi:[1,0]
	v_pk_mul_f32 v[6:7], v[6:7], s[44:45] op_sel_hi:[1,0]
	v_pk_mul_f32 v[22:23], v[24:25], s[44:45] op_sel_hi:[1,0]
	v_pk_mul_f32 v[24:25], v[26:27], s[44:45] op_sel_hi:[1,0]
	v_pk_mul_f32 v[8:9], v[8:9], s[44:45] op_sel_hi:[1,0]
	v_pk_mul_f32 v[26:27], v[28:29], s[44:45] op_sel_hi:[1,0]
	v_pk_mul_f32 v[28:29], v[30:31], s[44:45] op_sel_hi:[1,0]
	v_bfe_u32 v31, v20, 16, 1
	v_bfe_u32 v34, v3, 16, 1
	v_bfe_u32 v38, v13, 16, 1
	v_bfe_u32 v39, v12, 16, 1
	v_bfe_u32 v43, v6, 16, 1
	v_bfe_u32 v46, v5, 16, 1
	v_bfe_u32 v35, v2, 16, 1
	v_add3_u32 v12, v12, v39, s85
	v_add3_u32 v13, v13, v38, s85
	v_add3_u32 v3, v3, v34, s85
	v_add3_u32 v20, v20, v31, s85
	v_add3_u32 v31, v5, v46, s85
	v_add3_u32 v34, v6, v43, s85
	v_bfe_u32 v5, v9, 16, 1
	v_bfe_u32 v6, v8, 16, 1
	v_pk_mul_f32 v[10:11], v[10:11], s[44:45] op_sel_hi:[1,0]
	v_bfe_u32 v30, v21, 16, 1
	v_bfe_u32 v36, v19, 16, 1
	v_bfe_u32 v37, v18, 16, 1
	v_bfe_u32 v47, v4, 16, 1
	v_add3_u32 v2, v2, v35, s85
	v_perm_b32 v128, v13, v12, s86
	v_add3_u32 v12, v8, v6, s85
	v_add3_u32 v13, v9, v5, s85
	s_waitcnt vmcnt(0)
	v_and_b32_e32 v9, 0xffff0000, v17
	v_lshlrev_b32_e32 v8, 16, v17
	v_bfe_u32 v42, v7, 16, 1
	v_add3_u32 v18, v18, v37, s85
	v_add3_u32 v19, v19, v36, s85
	v_add3_u32 v21, v21, v30, s85
	v_add3_u32 v30, v4, v47, s85
	v_perm_b32 v130, v3, v2, s86
	v_bfe_u32 v2, v10, 16, 1
	v_bfe_u32 v3, v27, 16, 1
	v_bfe_u32 v4, v26, 16, 1
	v_pk_mul_f32 v[8:9], v[8:9], s[44:45] op_sel_hi:[1,0]
	v_add3_u32 v35, v7, v42, s85
	v_perm_b32 v129, v19, v18, s86
	v_add3_u32 v18, v26, v4, s85
	v_add3_u32 v19, v27, v3, s85
	v_add3_u32 v10, v10, v2, s85
	v_and_b32_e32 v3, 0xffff0000, v14
	v_lshlrev_b32_e32 v2, 16, v14
	v_and_b32_e32 v5, 0xffff0000, v15
	v_lshlrev_b32_e32 v4, 16, v15
	v_and_b32_e32 v7, 0xffff0000, v16
	v_lshlrev_b32_e32 v6, 16, v16
	v_bfe_u32 v14, v9, 16, 1
	v_pk_mul_f32 v[4:5], v[4:5], s[44:45] op_sel_hi:[1,0]
	v_pk_mul_f32 v[6:7], v[6:7], s[44:45] op_sel_hi:[1,0]
	v_bfe_u32 v15, v8, 16, 1
	v_add3_u32 v9, v9, v14, s85
	v_bfe_u32 v14, v1, 3, 3
	v_bfe_u32 v16, v7, 16, 1
	v_bfe_u32 v17, v6, 16, 1
	v_bfe_u32 v27, v4, 16, 1
	v_add3_u32 v8, v8, v15, s85
	v_or_b32_e32 v15, s80, v14
	v_bfe_u32 v26, v5, 16, 1
	v_add3_u32 v4, v4, v27, s85
	v_add3_u32 v6, v6, v17, s85
	v_add3_u32 v7, v7, v16, s85
	v_lshrrev_b32_e32 v16, 1, v15
	v_bfe_u32 v17, v1, 4, 2
	v_lshrrev_b32_e32 v27, 2, v1
	v_add3_u32 v5, v5, v26, s85
	v_xor_b32_e32 v16, v16, v1
	v_or_b32_e32 v26, s80, v17
	v_xor_b32_e32 v17, v27, v17
	v_lshlrev_b32_e32 v16, 4, v16
	v_lshlrev_b32_e32 v17, 6, v17
	v_lshlrev_b32_e32 v27, 4, v1
	v_lshlrev_b32_e32 v15, 12, v15
	v_and_b32_e32 v17, 0xc0, v17
	v_and_b32_e32 v27, 48, v27
	v_and_or_b32 v152, v16, s1, v15
	v_lshlrev_b32_e32 v15, 12, v26
	v_or3_b32 v153, v27, v17, v15
	v_lshlrev_b32_e32 v15, 2, v1
	v_lshrrev_b32_e32 v16, 1, v1
	v_bfe_u32 v17, v1, 1, 3
	v_bfe_u32 v26, v1, 2, 2
	v_and_b32_e32 v1, 16, v1
	v_and_or_b32 v1, v15, 12, v1
	v_lshl_add_u32 v15, v32, 7, 0
	v_bitop3_b32 v16, v33, v16, 7 bitop3:0x78
	v_and_or_b32 v14, v14, 4, v26
	v_lshl_add_u32 v155, v16, 4, v15
	v_bitop3_b32 v16, v33, v17, 2 bitop3:0x36
	v_lshl_add_u32 v156, v16, 4, v15
	v_bitop3_b32 v16, v33, v17, 4 bitop3:0x36
	v_lshlrev_b32_e32 v14, 8, v14
	v_lshlrev_b32_e32 v1, 1, v1
	v_lshl_add_u32 v157, v16, 4, v15
	v_bitop3_b32 v16, v33, v17, 6 bitop3:0x36
	v_add3_u32 v1, 0, v14, v1
	v_lshlrev_b32_e32 v14, 6, v26
	v_lshl_add_u32 v158, v16, 4, v15
	v_xor_b32_e32 v15, 64, v14
	v_add3_u32 v159, v1, v14, s87
	v_add3_u32 v160, v1, v15, s87
	v_xor_b32_e32 v15, 0x80, v14
	v_xor_b32_e32 v14, 0xc0, v14
	v_add3_u32 v161, v1, v15, s87
	v_add3_u32 v162, v1, v14, s87
	s_mov_b32 m0, s92
	s_nop 0
	global_load_lds_dwordx4 v152, s[64:65]
	v_or_b32_e32 v154, 0x4000, v153
	s_mov_b32 m0, s76
	s_nop 0
	global_load_lds_dwordx4 v153, s[48:49]
	v_bfe_u32 v48, v29, 16, 1
	s_mov_b32 m0, s77
	s_nop 0
	global_load_lds_dwordx4 v154, s[48:49]
	s_add_u32 s0, s64, 0x40000
	s_addc_u32 s1, s65, 0
	s_add_i32 s78, s92, 0x2000
	s_mov_b32 m0, s78
	s_nop 0
	global_load_lds_dwordx4 v152, s[0:1]
	s_add_i32 s36, s75, 0xc000
	s_mov_b32 m0, s36
	s_nop 0
	global_load_lds_dwordx4 v153, s[56:57]
	v_bfe_u32 v49, v28, 16, 1
	v_pk_mul_f32 v[2:3], v[2:3], s[44:45] op_sel_hi:[1,0]
	s_add_i32 s37, s75, 0xc400
	s_mov_b32 m0, s37
	s_nop 0
	global_load_lds_dwordx4 v154, s[56:57]
	v_bfe_u32 v40, v25, 16, 1
	v_bfe_u32 v41, v24, 16, 1
	v_bfe_u32 v44, v23, 16, 1
	v_bfe_u32 v45, v22, 16, 1
	v_bfe_u32 v50, v11, 16, 1
	v_perm_b32 v131, v21, v20, s86
	v_add3_u32 v20, v28, v49, s85
	v_add3_u32 v21, v29, v48, s85
	v_bfe_u32 v28, v3, 16, 1
	v_bfe_u32 v29, v2, 16, 1
	s_waitcnt vmcnt(0)
	v_add3_u32 v22, v22, v45, s85
	v_add3_u32 v23, v23, v44, s85
	v_add3_u32 v24, v24, v41, s85
	v_add3_u32 v25, v25, v40, s85
	v_add3_u32 v11, v11, v50, s85
	v_add3_u32 v2, v2, v29, s85
	v_add3_u32 v3, v3, v28, s85
	s_waitcnt lgkmcnt(0)
	s_barrier
; template <int MODE, int DQK, int DV>
; __device__ __forceinline__ void attn_pass(LAS unsigned char* lds, const Tens& T, size_t rowbase, int q0, f32x16 (&o)[DV / 32], float& l_out, const int wave, QPre* qp = nullptr) {
;     ...
;     float m = -64.0f, l = 0.f;
;     bf16x8 kone = {0, 0, 0, 0, 0, 0, 0, 0}, qm = kone;
;     if (MODE == AM_DSA) { if (h == 0) { kone[0] = (short)0x3F80; kone[1] = (short)0x3F80; kone[2] = (short)0x3F80; } qm = split3_bf16(64.0f, h); }
;     f32x16 negm;
; #pragma unroll
;     for (int rg = 0; rg < 16; ++rg) negm[rg] = 64.0f;
; #pragma unroll
;     for (int i = 0; i < NDB; ++i) o[i] = f32x16{};
	v_perm_b32 v132, v31, v30, s86
	v_mov_b32_e32 v14, v0
	v_mov_b32_e32 v15, v0
	v_mov_b32_e32 v30, v145
	v_mov_b32_e32 v31, v145
	v_perm_b32 v135, v25, v24, s86
	v_perm_b32 v134, v35, v34, s86
	v_perm_b32 v133, v23, v22, s86
	v_perm_b32 v139, v21, v20, s86
	v_perm_b32 v138, v11, v10, s86
	v_perm_b32 v137, v19, v18, s86
	v_perm_b32 v136, v13, v12, s86
	v_perm_b32 v143, v9, v8, s86
	v_perm_b32 v142, v7, v6, s86
	v_perm_b32 v141, v5, v4, s86
	v_perm_b32 v140, v3, v2, s86
	v_mov_b32_e32 v1, v0
	v_mov_b32_e32 v2, v0
	v_mov_b32_e32 v3, v0
	v_mov_b32_e32 v4, v0
	v_mov_b32_e32 v5, v0
	v_mov_b32_e32 v6, v0
	v_mov_b32_e32 v7, v0
	v_mov_b32_e32 v8, v0
	v_mov_b32_e32 v9, v0
	v_mov_b32_e32 v10, v0
	v_mov_b32_e32 v11, v0
	v_mov_b32_e32 v12, v0
	v_mov_b32_e32 v13, v0
	v_mov_b32_e32 v16, v145
	v_mov_b32_e32 v17, v145
	v_mov_b32_e32 v18, v145
	v_mov_b32_e32 v19, v145
	v_mov_b32_e32 v20, v145
	v_mov_b32_e32 v21, v145
	v_mov_b32_e32 v22, v145
	v_mov_b32_e32 v23, v145
	v_mov_b32_e32 v24, v145
	v_mov_b32_e32 v25, v145
	v_mov_b32_e32 v26, v145
	v_mov_b32_e32 v27, v145
	v_mov_b32_e32 v28, v145
	v_mov_b32_e32 v29, v145
	v_mov_b64_e32 v[78:79], v[30:31]
	v_mov_b64_e32 v[62:63], v[30:31]
	v_mov_b64_e32 v[46:47], v[30:31]
	v_mov_b64_e32 v[94:95], v[14:15]
	s_mov_b32 s0, 0
	v_mov_b64_e32 v[76:77], v[28:29]
	v_mov_b64_e32 v[74:75], v[26:27]
	v_mov_b64_e32 v[72:73], v[24:25]
	v_mov_b64_e32 v[70:71], v[22:23]
	v_mov_b64_e32 v[68:69], v[20:21]
	v_mov_b64_e32 v[66:67], v[18:19]
	v_mov_b64_e32 v[64:65], v[16:17]
	v_mov_b64_e32 v[60:61], v[28:29]
	v_mov_b64_e32 v[58:59], v[26:27]
	v_mov_b64_e32 v[56:57], v[24:25]
	v_mov_b64_e32 v[54:55], v[22:23]
	v_mov_b64_e32 v[52:53], v[20:21]
	v_mov_b64_e32 v[50:51], v[18:19]
	v_mov_b64_e32 v[48:49], v[16:17]
	v_mov_b64_e32 v[44:45], v[28:29]
	v_mov_b64_e32 v[42:43], v[26:27]
	v_mov_b64_e32 v[40:41], v[24:25]
	v_mov_b64_e32 v[38:39], v[22:23]
	v_mov_b64_e32 v[36:37], v[20:21]
	v_mov_b64_e32 v[34:35], v[18:19]
	v_mov_b64_e32 v[32:33], v[16:17]
	v_mov_b64_e32 v[92:93], v[12:13]
	v_mov_b64_e32 v[90:91], v[10:11]
	v_mov_b64_e32 v[88:89], v[8:9]
	v_mov_b64_e32 v[86:87], v[6:7]
	v_mov_b64_e32 v[84:85], v[4:5]
	v_mov_b64_e32 v[82:83], v[2:3]
	v_mov_b64_e32 v[80:81], v[0:1]
	s_branch .LBB0_2441

; #define ATT_ISSUE(st_, sl) do { _Pragma("unroll") for (int sb_ = 0; sb_ < NSUB; ++sb_) ATT_DMA(ATT_TILE((st_) * NSUB + sb_), sl, sb_); } while (0)
; template <int MODE, int DQK, int DV>
; __device__ __forceinline__ void attn_pass(LAS unsigned char* lds, const Tens& T, size_t rowbase, int q0, f32x16 (&o)[DV / 32], float& l_out, const int wave, QPre* qp = nullptr) {
;     ...
;         { constexpr int sl2 = (sl + NRING - 1) % NRING; if (st + NRING - 1 < nst) ATT_ISSUE(st + NRING - 1, sl2); }
.LBB0_2444:
	s_lshl_b32 s34, s1, 1
	s_lshl_b64 s[2:3], s[34:35], 18
	s_add_u32 s4, s64, s2
	s_addc_u32 s5, s65, s3
	s_add_i32 s6, s92, 0x4000
	s_mov_b32 m0, s6
	s_nop 0
	global_load_lds_dwordx4 v152, s[4:5]
	s_add_u32 s2, s48, s2
	s_addc_u32 s3, s49, s3
	s_add_i32 s4, s75, 0x10000
	s_mov_b32 m0, s4
	s_nop 0
	global_load_lds_dwordx4 v153, s[2:3]
	s_or_b32 s34, s34, 1
	s_add_i32 s4, s75, 0x10400
	s_mov_b32 m0, s4
	s_nop 0
	global_load_lds_dwordx4 v154, s[2:3]
	s_lshl_b64 s[2:3], s[34:35], 18
	s_add_u32 s4, s64, s2
	s_addc_u32 s5, s65, s3
	s_add_i32 s6, s92, 0x6000
	s_mov_b32 m0, s6
	s_nop 0
	global_load_lds_dwordx4 v152, s[4:5]
	s_add_u32 s2, s48, s2
	s_addc_u32 s3, s49, s3
	s_add_i32 s4, s75, 0x14000
	s_mov_b32 m0, s4
	s_nop 0
	global_load_lds_dwordx4 v153, s[2:3]
	s_add_i32 s4, s75, 0x14400
	s_mov_b32 m0, s4
	s_nop 0
	global_load_lds_dwordx4 v154, s[2:3]
	s_lshl_b32 s34, s0, 1
	s_cmp_gt_u32 s34, s83
	s_cbranch_scc1 .LBB0_2443

; #define ATT_ISSUE(st_, sl) do { _Pragma("unroll") for (int sb_ = 0; sb_ < NSUB; ++sb_) ATT_DMA(ATT_TILE((st_) * NSUB + sb_), sl, sb_); } while (0)
; template <int MODE, int DQK, int DV>
; __device__ __forceinline__ void attn_pass(LAS unsigned char* lds, const Tens& T, size_t rowbase, int q0, f32x16 (&o)[DV / 32], float& l_out, const int wave, QPre* qp = nullptr) {
;     ...
;         { constexpr int sl2 = (sl + NRING - 1) % NRING; if (st + NRING - 1 < nst) ATT_ISSUE(st + NRING - 1, sl2); }
.LBB0_2472:
	s_lshl_b32 s34, s0, 1
	s_lshl_b64 s[2:3], s[34:35], 18
	s_add_u32 s4, s64, s2
	s_addc_u32 s5, s65, s3
	s_mov_b32 m0, s92
	s_nop 0
	global_load_lds_dwordx4 v152, s[4:5]
	s_add_u32 s2, s48, s2
	s_addc_u32 s3, s49, s3
	s_mov_b32 m0, s76
	s_nop 0
	global_load_lds_dwordx4 v153, s[2:3]
	s_or_b32 s34, s34, 1
	s_mov_b32 m0, s77
	s_nop 0
	global_load_lds_dwordx4 v154, s[2:3]
	s_lshl_b64 s[2:3], s[34:35], 18
	s_add_u32 s4, s64, s2
	s_addc_u32 s5, s65, s3
	s_mov_b32 m0, s78
	s_nop 0
	global_load_lds_dwordx4 v152, s[4:5]
	s_add_u32 s2, s48, s2
	s_addc_u32 s3, s49, s3
	s_mov_b32 m0, s36
	s_nop 0
	global_load_lds_dwordx4 v153, s[2:3]
	s_nop 0
	s_mov_b32 m0, s37
	s_nop 0
	global_load_lds_dwordx4 v154, s[2:3]
	s_lshl_b32 s34, s1, 1
	s_cmp_gt_u32 s34, s83
	s_cbranch_scc1 .LBB0_2470

; template <int MODE, int DQK, int DV>
; __device__ __forceinline__ void attn_pass(LAS unsigned char* lds, const Tens& T, size_t rowbase, int q0, f32x16 (&o)[DV / 32], float& l_out, const int wave, QPre* qp = nullptr) {
;     ...
;         const bf16* qp = T.Q + (rowbase + tq) * (size_t)T.ldq + 8 * h;
; #pragma unroll
;         for (int s = 0; s < NSTEP; ++s) qf[s] = *(const bf16x8*)(qp + 16 * s);
;     }
;     {
;         f32x4 c0 = {1.f, 1.f, 1.f, 1.f}, c1 = c0, s0 = {0.f, 0.f, 0.f, 0.f}, s1 = s0;
;         if (MODE == AM_MLA) {
;             c0 = *(const f32x4*)(T.rcos + tq * 16 + 8 * h); c1 = *(const f32x4*)(T.rcos + tq * 16 + 8 * h + 4);
;             s0 = *(const f32x4*)(T.rsin + tq * 16 + 8 * h); s1 = *(const f32x4*)(T.rsin + tq * 16 + 8 * h + 4);
;     ...
;     const int nvm = 1 + ((DQK == 96 && wave < 4) ? 1 : 0) + DV / 64 + ((MODE == AM_FOX && wave == 0) ? 1 : 0) + ((MODE == AM_DSA) ? 1 : 0);
;     ...
;     const unsigned koff = (unsigned)(r * 128), kswz = (unsigned)((r >> 1) & 7);
;     const unsigned roff = (unsigned)(8192 + r * 64), rswz = (unsigned)((r >> 2) & 3);
;     const int g16 = lane >> 4, qq = (lane & 15) >> 2, pp = lane & 3;
;     const int vsw = (DV == 64) ? ((qq >> 1) & 1) : qq;
;     const unsigned voff = (unsigned)((4 * (g16 >> 1) + qq) * VROW + (16 * (g16 & 1) + 4 * pp) * 2);
;     const LAS unsigned char* kfa[NSTEP]; const LAS unsigned char* vfa[NDB];
; #pragma unroll
;     for (int s = 0; s < NSTEP; ++s) {
;         kfa[s] = (s < 4) ? lds + OFF_K + koff + (((unsigned)(2 * s + h) ^ kswz) * 16) : lds + OFF_K + roff + (((unsigned)(2 * (s - 4) + h) ^ rswz) * 16);
;         asm volatile("" : "+v"(kfa[s]));
;     }
; #pragma unroll
;     for (int db = 0; db < NDB; ++db) { vfa[db] = lds + OFF_V + voff + (unsigned)((db ^ vsw) * 64); asm volatile("" : "+v"(vfa[db])); }
;     float m = -64.0f, l = 0.f;
;     bf16x8 kone = {0, 0, 0, 0, 0, 0, 0, 0}, qm = kone;
;     if (MODE == AM_DSA) { if (h == 0) { kone[0] = (short)0x3F80; kone[1] = (short)0x3F80; kone[2] = (short)0x3F80; } qm = split3_bf16(64.0f, h); }
;     f32x16 negm;
; #pragma unroll
;     for (int rg = 0; rg < 16; ++rg) negm[rg] = 64.0f;
; #pragma unroll
;     for (int i = 0; i < NDB; ++i) o[i] = f32x16{};
;     const int jlast = (q0 + wave * 32) / 64;
;     constexpr bool DESC = (MODE == AM_FOX);
;     ...
;     bool wdone = false;
;     volatile LAS int* dflag = (volatile LAS int*)(lds + OFF_MISC + 16);
.LBB0_2518:
	v_add_u32_e32 v0, 0, v0
	s_waitcnt lgkmcnt(0)
	s_barrier
	ds_read_b32 v0, v0
	s_waitcnt lgkmcnt(0)
	s_barrier
	v_readfirstlane_b32 s1, v0
	s_cmp_lt_i32 s1, 0
	s_cbranch_scc1 .LBB0_2649
	s_bfe_u32 s92, s1, 0x30005
	s_lshr_b32 s46, s1, 8
	s_mul_i32 s4, s92, 0xc0
	v_readlane_b32 s5, v254, 8
	s_add_u32 s4, s5, s4
	v_readlane_b32 s5, v254, 57
	s_addc_u32 s5, s5, 0
	s_lshl_b32 s6, s92, 8
	v_readlane_b32 s7, v254, 59
	s_add_u32 s6, s7, s6
	v_readlane_b32 s7, v254, 30
	s_addc_u32 s7, s7, 0
	s_not_b32 s1, s1
	s_lshl_b32 s1, s1, 8
	s_and_b32 s95, s1, 0x1f00
	v_mbcnt_lo_u32_b32 v15, -1, 0
	v_mbcnt_hi_u32_b32 v15, -1, v15
	s_add_i32 s96, s95, s78
	v_and_b32_e32 v47, 31, v15
	s_lshl_b64 s[56:57], s[46:47], 13
	v_or_b32_e32 v0, s96, v47
	v_lshl_add_u64 v[2:3], s[56:57], 0, v[0:1]
	v_mov_b64_e32 v[4:5], s[4:5]
	s_movk_i32 s1, 0x600
	v_bfe_u32 v14, v15, 5, 1
	v_mad_u64_u32 v[4:5], s[4:5], v2, s1, v[4:5]
	v_mad_u32_u24 v5, v3, s1, v5
	v_lshlrev_b32_e32 v2, 4, v14
	v_mov_b32_e32 v3, v1
	v_lshl_add_u64 v[2:3], v[4:5], 0, v[2:3]
	global_load_dwordx4 v[42:45], v[2:3], off
	global_load_dwordx4 v[38:41], v[2:3], off offset:32
	global_load_dwordx4 v[34:37], v[2:3], off offset:64
	global_load_dwordx4 v[30:33], v[2:3], off offset:96
	global_load_dwordx4 v[10:13], v[2:3], off offset:128
	global_load_dwordx4 v[6:9], v[2:3], off offset:160
	v_lshlrev_b32_e32 v2, 4, v0
	v_mov_b32_e32 v3, v1
	v_lshlrev_b64 v[18:19], 2, v[2:3]
	v_lshl_add_u64 v[2:3], s[40:41], 0, v[18:19]
	v_and_b32_e32 v20, 32, v15
	v_mov_b32_e32 v21, v1
	v_lshl_add_u64 v[18:19], s[42:43], 0, v[18:19]
	v_lshl_add_u64 v[22:23], v[2:3], 0, v[20:21]
	v_lshl_add_u64 v[26:27], v[18:19], 0, v[20:21]
	global_load_dwordx4 v[2:5], v[22:23], off offset:16
	s_nop 0
	global_load_dwordx4 v[22:25], v[22:23], off
	s_nop 0
	global_load_dwordx4 v[18:21], v[26:27], off offset:16
	s_nop 0
	global_load_dwordx4 v[26:29], v[26:27], off
	v_bfe_u32 v48, v15, 3, 3
	v_or_b32_e32 v17, s79, v48
	v_lshrrev_b32_e32 v46, 1, v17
	v_xor_b32_e32 v46, v46, v15
	v_lshlrev_b32_e32 v49, 3, v46
	v_bfe_u32 v46, v15, 2, 4
	v_lshlrev_b32_e32 v50, 4, v15
	v_bitop3_b32 v50, v50, 48, v15 bitop3:0x48
	v_lshlrev_b32_e32 v51, 6, v46
	v_or3_b32 v143, v50, v51, s80
	v_lshlrev_b32_e32 v50, 2, v15
	v_lshlrev_b32_e32 v47, 6, v47
	v_and_b32_e32 v55, 16, v15
	v_lshrrev_b32_e32 v51, 1, v15
	v_and_or_b32 v50, v50, 12, v55
	v_add_u32_e32 v55, 0, v47
	v_bfe_u32 v52, v15, 1, 3
	v_add_u32_e32 v47, v55, v47
	v_bitop3_b32 v51, v14, v51, 7 bitop3:0x78
	v_lshl_add_u32 v144, v51, 4, v47
	v_bitop3_b32 v51, v14, v52, 2 bitop3:0x36
	v_lshl_add_u32 v145, v51, 4, v47
	v_bitop3_b32 v51, v14, v52, 4 bitop3:0x36
	v_lshrrev_b32_e32 v53, 2, v15
	v_lshl_add_u32 v146, v51, 4, v47
	v_bitop3_b32 v51, v14, v52, 6 bitop3:0x36
	v_lshl_add_u32 v147, v51, 4, v47
	v_bitop3_b32 v47, v14, v53, 3 bitop3:0x78
	v_bfe_u32 v54, v15, 2, 2
	v_lshlrev_b32_e32 v47, 4, v47
	s_movk_i32 s1, 0x2000
	v_add3_u32 v148, v55, v47, s1
	v_bitop3_b32 v47, v14, v54, 2 bitop3:0x36
	v_and_or_b32 v48, v48, 4, v54
	v_lshlrev_b32_e32 v47, 4, v47
	s_lshl_b64 s[4:5], s[46:47], 24
	v_add3_u32 v149, v55, v47, s1
	v_lshlrev_b32_e32 v47, 7, v48
	v_lshlrev_b32_e32 v48, 1, v50
	s_add_u32 s58, s6, s4
	v_add3_u32 v47, s87, v47, v48
	v_lshlrev_b32_e32 v48, 3, v15
	v_lshlrev_b32_e32 v17, 10, v17
	s_addc_u32 s59, s7, s5
	s_lshl_b64 s[4:5], s[46:47], 19
	v_readlane_b32 s1, v254, 31
	v_and_b32_e32 v48, 64, v48
	v_and_or_b32 v49, v49, 56, v17
	s_add_u32 s60, s1, s4
	v_readlane_b32 s1, v254, 33
	v_add_u32_e32 v151, v47, v48
	v_xad_u32 v152, v48, 64, v47
	v_lshlrev_b32_e32 v150, 1, v49
	s_addc_u32 s61, s1, s5
	s_mov_b32 m0, s88
	s_nop 0
	global_load_lds_dwordx4 v150, s[58:59]
	s_and_b64 vcc, exec, s[2:3]
	s_cbranch_vccnz .LBB0_2521
	s_mov_b32 m0, s89
	s_nop 0
	global_load_lds_dwordx4 v143, s[60:61]
.LBB0_2521:
	v_and_b32_e32 v15, 63, v15
	v_lshrrev_b32_e32 v47, 4, v15
	v_xor_b32_e32 v46, v46, v47
	v_lshlrev_b32_e32 v46, 5, v46
	v_lshlrev_b32_e32 v47, 3, v15
	v_and_b32_e32 v46, 32, v46
	v_and_b32_e32 v47, 24, v47
	s_add_u32 s62, s58, 0x80
	v_or3_b32 v17, v47, v46, v17
	s_addc_u32 s63, s59, 0
	v_lshlrev_b32_e32 v153, 1, v17
	s_mov_b32 m0, s91
	s_nop 0
	global_load_lds_dwordx4 v153, s[62:63]
	s_add_u32 s4, s58, 0x20000
	s_addc_u32 s5, s59, 0
	s_mov_b32 m0, s93
	s_nop 0
	global_load_lds_dwordx4 v150, s[4:5]
	s_and_b64 vcc, exec, s[2:3]
	s_cbranch_vccnz .LBB0_2523
	s_add_u32 s4, s60, 0x1000
	s_addc_u32 s5, s61, 0
	s_add_i32 s1, s88, 0x5000
	s_mov_b32 m0, s1
	s_nop 0
	global_load_lds_dwordx4 v143, s[4:5]
.LBB0_2523:
	s_add_u32 s4, s62, 0x20000
	s_addc_u32 s5, s63, 0
	s_add_i32 s97, s88, 0x14000
	s_mov_b32 m0, s97
	s_nop 0
	global_load_lds_dwordx4 v153, s[4:5]
	s_add_u32 s4, s58, 0x40000
	s_addc_u32 s5, s59, 0
	s_add_i32 s82, s88, 0x6000
	s_mov_b32 m0, s82
	s_nop 0
	global_load_lds_dwordx4 v150, s[4:5]
	s_and_b64 vcc, exec, s[2:3]
	s_cbranch_vccnz .LBB0_2525
	s_add_u32 s4, s60, 0x2000
	s_addc_u32 s5, s61, 0
	s_add_i32 s1, s88, 0x8000
	s_mov_b32 m0, s1
	s_nop 0
	global_load_lds_dwordx4 v143, s[4:5]
.LBB0_2525:
	s_add_u32 s4, s62, 0x40000
	s_addc_u32 s5, s63, 0
	s_mov_b32 m0, s94
	s_nop 0
	global_load_lds_dwordx4 v153, s[4:5]
	s_add_u32 s4, s58, 0x60000
	s_addc_u32 s5, s59, 0
	s_add_i32 s83, s88, 0x9000
	s_mov_b32 m0, s83
	s_nop 0
	global_load_lds_dwordx4 v150, s[4:5]
	s_and_b64 vcc, exec, s[2:3]
	s_cbranch_vccnz .LBB0_2527
	s_add_u32 s4, s60, 0x3000
	s_addc_u32 s5, s61, 0
	s_add_i32 s1, s88, 0xb000
	s_mov_b32 m0, s1
	s_nop 0
	global_load_lds_dwordx4 v143, s[4:5]
.LBB0_2527:
	s_add_u32 s4, s62, 0x60000
	s_addc_u32 s5, s63, 0
	s_add_i32 s33, s88, 0x18000
	s_mov_b32 m0, s33
	s_nop 0
	global_load_lds_dwordx4 v153, s[4:5]
	s_mov_b64 s[4:5], -1
	s_and_b64 vcc, exec, s[44:45]
	s_cbranch_vccz .LBB0_2529
	s_waitcnt vmcnt(6)
	s_mov_b64 s[4:5], 0

; #define ATT_ISSUE(st_, sl) do { _Pragma("unroll") for (int sb_ = 0; sb_ < NSUB; ++sb_) ATT_DMA(ATT_TILE((st_) * NSUB + sb_), sl, sb_); } while (0)
; template <int MODE, int DQK, int DV>
; __device__ __forceinline__ void attn_pass(LAS unsigned char* lds, const Tens& T, size_t rowbase, int q0, f32x16 (&o)[DV / 32], float& l_out, const int wave, QPre* qp = nullptr) {
;     ...
;         { constexpr int sl2 = (sl + NRING - 1) % NRING; if (st + NRING - 1 < nst) ATT_ISSUE(st + NRING - 1, sl2); }
.LBB0_2534:
	s_add_i32 s0, s76, 2
	s_cmp_lt_u32 s0, s49
	s_cselect_b64 s[68:69], -1, 0
	s_cmp_ge_u32 s0, s49
	s_cselect_b64 s[66:67], -1, 0
	s_and_b64 vcc, exec, s[66:67]
	s_cbranch_vccnz .LBB0_2540
	s_lshl_b32 s46, s0, 1
	s_lshl_b64 s[6:7], s[46:47], 17
	s_add_u32 s8, s58, s6
	s_addc_u32 s9, s59, s7
	s_add_i32 s1, s88, 0xc000
	s_mov_b32 m0, s1
	s_nop 0
	global_load_lds_dwordx4 v150, s[8:9]
	s_and_b64 vcc, exec, s[2:3]
	s_cbranch_vccnz .LBB0_2537
	s_lshl_b64 s[8:9], s[46:47], 12
	s_add_u32 s8, s60, s8
	s_addc_u32 s9, s61, s9
	s_add_i32 s1, s88, 0xe000
	s_mov_b32 m0, s1
	s_nop 0
	global_load_lds_dwordx4 v143, s[8:9]
.LBB0_2537:
	s_add_u32 s6, s62, s6
	s_addc_u32 s7, s63, s7
	s_or_b32 s46, s46, 1
	s_add_i32 s1, s88, 0x1a000
	s_mov_b32 m0, s1
	s_nop 0
	global_load_lds_dwordx4 v153, s[6:7]
	s_lshl_b64 s[6:7], s[46:47], 17
	s_add_u32 s8, s58, s6
	s_addc_u32 s9, s59, s7
	s_add_i32 s1, s88, 0xf000
	s_mov_b32 m0, s1
	s_nop 0
	global_load_lds_dwordx4 v150, s[8:9]
	s_and_b64 vcc, exec, s[2:3]
	s_cbranch_vccnz .LBB0_2539
	s_lshl_b64 s[8:9], s[46:47], 12
	s_add_u32 s8, s60, s8
	s_addc_u32 s9, s61, s9
	s_add_i32 s1, s88, 0x11000
	s_mov_b32 m0, s1
	s_nop 0
	global_load_lds_dwordx4 v143, s[8:9]
.LBB0_2539:
	s_add_u32 s6, s62, s6
	s_addc_u32 s7, s63, s7
	s_add_i32 s1, s88, 0x1c000
	s_mov_b32 m0, s1
	s_nop 0
	global_load_lds_dwordx4 v153, s[6:7]

; #define ATT_ISSUE(st_, sl) do { _Pragma("unroll") for (int sb_ = 0; sb_ < NSUB; ++sb_) ATT_DMA(ATT_TILE((st_) * NSUB + sb_), sl, sb_); } while (0)
; template <int MODE, int DQK, int DV>
; __device__ __forceinline__ void attn_pass(LAS unsigned char* lds, const Tens& T, size_t rowbase, int q0, f32x16 (&o)[DV / 32], float& l_out, const int wave, QPre* qp = nullptr) {
;     ...
;         { constexpr int sl2 = (sl + NRING - 1) % NRING; if (st + NRING - 1 < nst) ATT_ISSUE(st + NRING - 1, sl2); }
.LBB0_2571:
	s_waitcnt lgkmcnt(0)
	s_barrier
	s_add_i32 s1, s76, 1
	s_cmp_ge_u32 s1, s49
	s_cbranch_scc1 .LBB0_2532
	s_add_i32 s77, s76, 3
	s_cmp_ge_u32 s77, s49
	s_cselect_b64 s[66:67], -1, 0
	s_and_b64 vcc, exec, s[66:67]
	s_cbranch_vccnz .LBB0_2578
	s_lshl_b32 s46, s77, 1
	s_lshl_b64 s[6:7], s[46:47], 17
	s_add_u32 s8, s58, s6
	s_addc_u32 s9, s59, s7
	s_mov_b32 m0, s88
	s_nop 0
	global_load_lds_dwordx4 v150, s[8:9]
	s_and_b64 vcc, exec, s[2:3]
	s_cbranch_vccnz .LBB0_2575
	s_lshl_b64 s[8:9], s[46:47], 12
	s_add_u32 s8, s60, s8
	s_addc_u32 s9, s61, s9
	s_mov_b32 m0, s89
	s_nop 0
	global_load_lds_dwordx4 v143, s[8:9]
.LBB0_2575:
	s_add_u32 s6, s62, s6
	s_addc_u32 s7, s63, s7
	s_or_b32 s46, s46, 1
	s_add_i32 s8, s88, 0x12000
	s_mov_b32 m0, s8
	s_nop 0
	global_load_lds_dwordx4 v153, s[6:7]
	s_lshl_b64 s[6:7], s[46:47], 17
	s_add_u32 s8, s58, s6
	s_addc_u32 s9, s59, s7
	s_mov_b32 m0, s93
	s_nop 0
	global_load_lds_dwordx4 v150, s[8:9]
	s_and_b64 vcc, exec, s[2:3]
	s_cbranch_vccnz .LBB0_2577
	s_lshl_b64 s[8:9], s[46:47], 12
	s_add_u32 s8, s60, s8
	s_addc_u32 s9, s61, s9
	s_add_i32 s10, s88, 0x5000
	s_mov_b32 m0, s10
	s_nop 0
	global_load_lds_dwordx4 v143, s[8:9]
.LBB0_2577:
	s_add_u32 s6, s62, s6
	s_addc_u32 s7, s63, s7
	s_mov_b32 m0, s97
	s_nop 0
	global_load_lds_dwordx4 v153, s[6:7]

; #define ATT_ISSUE(st_, sl) do { _Pragma("unroll") for (int sb_ = 0; sb_ < NSUB; ++sb_) ATT_DMA(ATT_TILE((st_) * NSUB + sb_), sl, sb_); } while (0)
; template <int MODE, int DQK, int DV>
; __device__ __forceinline__ void attn_pass(LAS unsigned char* lds, const Tens& T, size_t rowbase, int q0, f32x16 (&o)[DV / 32], float& l_out, const int wave, QPre* qp = nullptr) {
;     ...
;         { constexpr int sl2 = (sl + NRING - 1) % NRING; if (st + NRING - 1 < nst) ATT_ISSUE(st + NRING - 1, sl2); }
.LBB0_2609:
	s_waitcnt lgkmcnt(0)
	s_barrier
	s_andn2_b64 vcc, exec, s[68:69]
	s_cbranch_vccnz .LBB0_2621
	s_add_i32 s76, s76, 4
	s_cmp_ge_u32 s76, s49
	s_cselect_b64 s[68:69], -1, 0
	s_and_b64 vcc, exec, s[68:69]
	s_cbranch_vccnz .LBB0_2616
	s_lshl_b32 s46, s76, 1
	s_lshl_b64 s[6:7], s[46:47], 17
	s_add_u32 s8, s58, s6
	s_addc_u32 s9, s59, s7
	s_mov_b32 m0, s82
	s_nop 0
	global_load_lds_dwordx4 v150, s[8:9]
	s_and_b64 vcc, exec, s[2:3]
	s_cbranch_vccnz .LBB0_2613
	s_lshl_b64 s[8:9], s[46:47], 12
	s_add_u32 s8, s60, s8
	s_addc_u32 s9, s61, s9
	s_add_i32 s1, s88, 0x8000
	s_mov_b32 m0, s1
	s_nop 0
	global_load_lds_dwordx4 v143, s[8:9]
.LBB0_2613:
	s_add_u32 s6, s62, s6
	s_addc_u32 s7, s63, s7
	s_or_b32 s46, s46, 1
	s_add_i32 s1, s88, 0x16000
	s_mov_b32 m0, s1
	s_nop 0
	global_load_lds_dwordx4 v153, s[6:7]
	s_lshl_b64 s[6:7], s[46:47], 17
	s_add_u32 s8, s58, s6
	s_addc_u32 s9, s59, s7
	s_mov_b32 m0, s83
	s_nop 0
	global_load_lds_dwordx4 v150, s[8:9]
	s_and_b64 vcc, exec, s[2:3]
	s_cbranch_vccnz .LBB0_2615
	s_lshl_b64 s[8:9], s[46:47], 12
	s_add_u32 s8, s60, s8
	s_addc_u32 s9, s61, s9
	s_add_i32 s1, s88, 0xb000
	s_mov_b32 m0, s1
	s_nop 0
	global_load_lds_dwordx4 v143, s[8:9]
.LBB0_2615:
	s_add_u32 s6, s62, s6
	s_addc_u32 s7, s63, s7
	s_mov_b32 m0, s33
	s_nop 0
	global_load_lds_dwordx4 v153, s[6:7]
